# speedup vs baseline: 1.0204x; 1.0143x over previous
.LBB4_12:
	s_add_u32 s81, s40, s22
	s_addc_u32 s82, s41, s23
	s_add_u32 s29, s40, 0x100
	s_addc_u32 s44, s41, 0
	s_and_b64 s[42:43], s[14:15], exec
	ds_read_b128 v[82:85], v161
	ds_read_b128 v[94:97], v161 offset:2048
	ds_read_b128 v[102:105], v162
	ds_read_b128 v[110:113], v162 offset:2048
	s_cselect_b32 s47, s37, s44
	s_cselect_b32 s46, s36, s29
	s_add_u32 s29, s38, 0x100
	s_addc_u32 s44, s39, 0
	s_and_b64 s[42:43], s[14:15], exec
	s_cselect_b32 s49, s5, s44
	s_cselect_b32 s48, s4, s29
	s_add_u32 s44, s46, 0x80
	s_addc_u32 s45, s47, 0
	s_add_u32 s42, s48, 0x80
	s_addc_u32 s43, s49, 0
	ds_read_b128 v[58:61], v163
	ds_read_b128 v[66:69], v163 offset:2048
	ds_read_b128 v[62:65], v164
	ds_read_b128 v[70:73], v164 offset:2048
	ds_read_b128 v[74:77], v163 offset:4096
	ds_read_b128 v[86:89], v163 offset:6144
	ds_read_b128 v[78:81], v164 offset:4096
	ds_read_b128 v[90:93], v164 offset:6144
	s_add_u32 s78, s81, 0x80
	s_addc_u32 s79, s82, 0
	s_mov_b32 m0, s70
	s_nop 0
	global_load_lds_dwordx4 v146, s[78:79]
	s_mov_b32 m0, s71
	s_nop 0
	global_load_lds_dwordx4 v150, s[78:79]
	ds_read_b128 v[142:145], v161 offset:16384
	ds_read_b128 v[166:169], v161 offset:18432
	ds_read_b128 v[170:173], v162 offset:16384
	ds_read_b128 v[174:177], v162 offset:18432
	s_waitcnt vmcnt(8)
	s_waitcnt lgkmcnt(0)
	s_barrier
	s_waitcnt lgkmcnt(0)
	s_waitcnt vmcnt(16)
	v_mov_b32_e32 v1, v0
	v_pk_mul_f32 v[16:17], v[0:1], v[16:17]
	v_pk_mul_f32 v[14:15], v[154:155], v[14:15]
	v_pk_mul_f32 v[12:13], v[0:1], v[12:13]
	v_pk_mul_f32 v[10:11], v[154:155], v[10:11]
	v_pk_mul_f32 v[8:9], v[0:1], v[8:9]
	v_pk_mul_f32 v[6:7], v[154:155], v[6:7]
	v_pk_mul_f32 v[4:5], v[0:1], v[4:5]
	v_pk_mul_f32 v[2:3], v[154:155], v[2:3]
	s_setprio 1
	s_waitcnt lgkmcnt(7)
	v_mfma_f32_16x16x128_f8f6f4 v[18:21], v[82:85], v[58:61], v[14:17] cbsz:4 blgp:4
	s_waitcnt lgkmcnt(5)
	v_mfma_f32_16x16x128_f8f6f4 v[18:21], v[102:105], v[62:65], v[18:21] cbsz:4 blgp:4
	v_mfma_f32_16x16x128_f8f6f4 v[22:25], v[94:97], v[58:61], v[10:13] cbsz:4 blgp:4
	s_nop 0
	v_mfma_f32_16x16x128_f8f6f4 v[22:25], v[110:113], v[62:65], v[22:25] cbsz:4 blgp:4
	v_mfma_f32_16x16x128_f8f6f4 v[26:29], v[82:85], v[66:69], v[14:17] cbsz:4 blgp:4
	s_waitcnt lgkmcnt(4)
	v_mfma_f32_16x16x128_f8f6f4 v[26:29], v[102:105], v[70:73], v[26:29] cbsz:4 blgp:4
	v_mfma_f32_16x16x128_f8f6f4 v[30:33], v[94:97], v[66:69], v[10:13] cbsz:4 blgp:4
	s_nop 0
	v_mfma_f32_16x16x128_f8f6f4 v[30:33], v[110:113], v[70:73], v[30:33] cbsz:4 blgp:4
	s_waitcnt lgkmcnt(3)
	v_mfma_f32_16x16x128_f8f6f4 v[34:37], v[82:85], v[74:77], v[14:17] cbsz:4 blgp:4
	s_waitcnt lgkmcnt(1)
	v_mfma_f32_16x16x128_f8f6f4 v[34:37], v[102:105], v[78:81], v[34:37] cbsz:4 blgp:4
	v_mfma_f32_16x16x128_f8f6f4 v[38:41], v[94:97], v[74:77], v[10:13] cbsz:4 blgp:4
	s_nop 0
	v_mfma_f32_16x16x128_f8f6f4 v[38:41], v[110:113], v[78:81], v[38:41] cbsz:4 blgp:4
	v_mfma_f32_16x16x128_f8f6f4 v[42:45], v[82:85], v[86:89], v[14:17] cbsz:4 blgp:4
	s_waitcnt lgkmcnt(0)
	v_mfma_f32_16x16x128_f8f6f4 v[42:45], v[102:105], v[90:93], v[42:45] cbsz:4 blgp:4
	v_mfma_f32_16x16x128_f8f6f4 v[46:49], v[94:97], v[86:89], v[10:13] cbsz:4 blgp:4
	s_nop 0
	v_mfma_f32_16x16x128_f8f6f4 v[46:49], v[110:113], v[90:93], v[46:49] cbsz:4 blgp:4
	s_waitcnt lgkmcnt(3)
	v_mfma_f32_16x16x128_f8f6f4 v[50:53], v[142:145], v[58:61], v[6:9] cbsz:4 blgp:4
	s_waitcnt lgkmcnt(1)
	v_mfma_f32_16x16x128_f8f6f4 v[50:53], v[170:173], v[62:65], v[50:53] cbsz:4 blgp:4
	v_mfma_f32_16x16x128_f8f6f4 v[54:57], v[166:169], v[58:61], v[2:5] cbsz:4 blgp:4
	s_waitcnt lgkmcnt(0)
	v_mfma_f32_16x16x128_f8f6f4 v[54:57], v[174:177], v[62:65], v[54:57] cbsz:4 blgp:4
	v_mfma_f32_16x16x128_f8f6f4 v[58:61], v[142:145], v[66:69], v[6:9] cbsz:4 blgp:4
	s_nop 0
	v_mfma_f32_16x16x128_f8f6f4 v[58:61], v[170:173], v[70:73], v[58:61] cbsz:4 blgp:4
	v_mfma_f32_16x16x128_f8f6f4 v[62:65], v[166:169], v[66:69], v[2:5] cbsz:4 blgp:4
	s_nop 0
	v_mfma_f32_16x16x128_f8f6f4 v[62:65], v[174:177], v[70:73], v[62:65] cbsz:4 blgp:4
	v_mfma_f32_16x16x128_f8f6f4 v[66:69], v[142:145], v[74:77], v[6:9] cbsz:4 blgp:4
	s_nop 0
	v_mfma_f32_16x16x128_f8f6f4 v[66:69], v[170:173], v[78:81], v[66:69] cbsz:4 blgp:4
	v_mfma_f32_16x16x128_f8f6f4 v[70:73], v[166:169], v[74:77], v[2:5] cbsz:4 blgp:4
	s_nop 0
	v_mfma_f32_16x16x128_f8f6f4 v[70:73], v[174:177], v[78:81], v[70:73] cbsz:4 blgp:4
	v_mfma_f32_16x16x128_f8f6f4 v[74:77], v[142:145], v[86:89], v[6:9] cbsz:4 blgp:4
	s_nop 0
	v_mfma_f32_16x16x128_f8f6f4 v[74:77], v[170:173], v[90:93], v[74:77] cbsz:4 blgp:4
	v_mfma_f32_16x16x128_f8f6f4 v[78:81], v[166:169], v[86:89], v[2:5] cbsz:4 blgp:4
	s_nop 0
	v_mfma_f32_16x16x128_f8f6f4 v[78:81], v[174:177], v[90:93], v[78:81] cbsz:4 blgp:4
	s_setprio 0
	s_barrier
	s_mov_b32 m0, s55
	s_nop 0
	global_load_lds_dwordx4 v148, s[48:49]
	s_mov_b32 m0, s56
	s_nop 0
	global_load_lds_dwordx4 v152, s[48:49]
	ds_read_b128 v[114:117], v163 offset:16384
	ds_read_b128 v[122:125], v163 offset:18432
	ds_read_b128 v[130:133], v164 offset:16384
	ds_read_b128 v[134:137], v164 offset:18432
	ds_read_b128 v[178:181], v163 offset:20480
	ds_read_b128 v[182:185], v163 offset:22528
	ds_read_b128 v[186:189], v164 offset:20480
	ds_read_b128 v[190:193], v164 offset:22528
	s_mov_b32 m0, s54
	s_nop 0
	global_load_lds_dwordx4 v146, s[46:47]
	s_mov_b32 m0, s57
	s_nop 0
	global_load_lds_dwordx4 v150, s[46:47]
	s_add_u32 s48, s48, s24
	s_addc_u32 s49, s49, s25
	s_mov_b32 m0, s58
	s_nop 0
	global_load_lds_dwordx4 v148, s[48:49]
	s_mov_b32 m0, s59
	s_nop 0
	global_load_lds_dwordx4 v152, s[48:49]
	s_waitcnt vmcnt(8)
	s_waitcnt lgkmcnt(0)
	s_barrier
	s_setprio 1
	s_waitcnt lgkmcnt(7)
	v_mfma_f32_16x16x128_f8f6f4 v[86:89], v[82:85], v[114:117], v[14:17] cbsz:4 blgp:4
	s_waitcnt lgkmcnt(5)
	v_mfma_f32_16x16x128_f8f6f4 v[86:89], v[102:105], v[130:133], v[86:89] cbsz:4 blgp:4
	v_mfma_f32_16x16x128_f8f6f4 v[90:93], v[94:97], v[114:117], v[10:13] cbsz:4 blgp:4
	s_nop 0
	v_mfma_f32_16x16x128_f8f6f4 v[90:93], v[110:113], v[130:133], v[90:93] cbsz:4 blgp:4
	v_mfma_f32_16x16x128_f8f6f4 v[98:101], v[82:85], v[122:125], v[14:17] cbsz:4 blgp:4
	s_waitcnt lgkmcnt(4)
	v_mfma_f32_16x16x128_f8f6f4 v[98:101], v[102:105], v[134:137], v[98:101] cbsz:4 blgp:4
	v_mfma_f32_16x16x128_f8f6f4 v[106:109], v[94:97], v[122:125], v[10:13] cbsz:4 blgp:4
	s_nop 0
	v_mfma_f32_16x16x128_f8f6f4 v[106:109], v[110:113], v[134:137], v[106:109] cbsz:4 blgp:4
	s_waitcnt lgkmcnt(3)
	v_mfma_f32_16x16x128_f8f6f4 v[118:121], v[82:85], v[178:181], v[14:17] cbsz:4 blgp:4
	s_waitcnt lgkmcnt(1)
	v_mfma_f32_16x16x128_f8f6f4 v[118:121], v[102:105], v[186:189], v[118:121] cbsz:4 blgp:4
	v_mfma_f32_16x16x128_f8f6f4 v[126:129], v[94:97], v[178:181], v[10:13] cbsz:4 blgp:4
	s_nop 0
	v_mfma_f32_16x16x128_f8f6f4 v[126:129], v[110:113], v[186:189], v[126:129] cbsz:4 blgp:4
	v_mfma_f32_16x16x128_f8f6f4 v[138:141], v[82:85], v[182:185], v[14:17] cbsz:4 blgp:4
	s_waitcnt lgkmcnt(0)
	v_mfma_f32_16x16x128_f8f6f4 v[138:141], v[102:105], v[190:193], v[138:141] cbsz:4 blgp:4
	v_mfma_f32_16x16x128_f8f6f4 v[82:85], v[94:97], v[182:185], v[10:13] cbsz:4 blgp:4
	s_nop 0
	v_mfma_f32_16x16x128_f8f6f4 v[82:85], v[110:113], v[190:193], v[82:85] cbsz:4 blgp:4
	v_mfma_f32_16x16x128_f8f6f4 v[94:97], v[142:145], v[114:117], v[6:9] cbsz:4 blgp:4
	s_nop 0
	v_mfma_f32_16x16x128_f8f6f4 v[94:97], v[170:173], v[130:133], v[94:97] cbsz:4 blgp:4
	v_mfma_f32_16x16x128_f8f6f4 v[102:105], v[166:169], v[114:117], v[2:5] cbsz:4 blgp:4
	s_nop 0
	v_mfma_f32_16x16x128_f8f6f4 v[102:105], v[174:177], v[130:133], v[102:105] cbsz:4 blgp:4
	v_mfma_f32_16x16x128_f8f6f4 v[110:113], v[142:145], v[122:125], v[6:9] cbsz:4 blgp:4
	s_nop 0
	v_mfma_f32_16x16x128_f8f6f4 v[110:113], v[170:173], v[134:137], v[110:113] cbsz:4 blgp:4
	v_mfma_f32_16x16x128_f8f6f4 v[114:117], v[166:169], v[122:125], v[2:5] cbsz:4 blgp:4
	s_nop 0
	v_mfma_f32_16x16x128_f8f6f4 v[114:117], v[174:177], v[134:137], v[114:117] cbsz:4 blgp:4
	v_mfma_f32_16x16x128_f8f6f4 v[122:125], v[142:145], v[178:181], v[6:9] cbsz:4 blgp:4
	s_nop 0
	v_mfma_f32_16x16x128_f8f6f4 v[122:125], v[170:173], v[186:189], v[122:125] cbsz:4 blgp:4
	v_mfma_f32_16x16x128_f8f6f4 v[130:133], v[166:169], v[178:181], v[2:5] cbsz:4 blgp:4
	s_nop 0
	v_mfma_f32_16x16x128_f8f6f4 v[130:133], v[174:177], v[186:189], v[130:133] cbsz:4 blgp:4
	v_mfma_f32_16x16x128_f8f6f4 v[134:137], v[142:145], v[182:185], v[6:9] cbsz:4 blgp:4
	s_nop 0
	v_mfma_f32_16x16x128_f8f6f4 v[134:137], v[170:173], v[190:193], v[134:137] cbsz:4 blgp:4
	v_mfma_f32_16x16x128_f8f6f4 v[142:145], v[166:169], v[182:185], v[2:5] cbsz:4 blgp:4
	s_nop 0
	v_mfma_f32_16x16x128_f8f6f4 v[142:145], v[174:177], v[190:193], v[142:145] cbsz:4 blgp:4
	s_setprio 0
	s_barrier
	ds_read_b128 v[166:169], v161 offset:32768
	ds_read_b128 v[170:173], v161 offset:34816
	ds_read_b128 v[174:177], v162 offset:32768
	ds_read_b128 v[178:181], v162 offset:34816
	ds_read_b128 v[182:185], v163 offset:32768
	ds_read_b128 v[186:189], v163 offset:34816
	ds_read_b128 v[190:193], v164 offset:32768
	ds_read_b128 v[194:197], v164 offset:34816
	ds_read_b128 v[198:201], v163 offset:36864
	ds_read_b128 v[202:205], v163 offset:38912
	ds_read_b128 v[206:209], v164 offset:36864
	ds_read_b128 v[210:213], v164 offset:38912
	s_add_u32 s46, s46, s22
	s_addc_u32 s47, s47, s23
	s_mov_b32 m0, s60
	s_nop 0
	global_load_lds_dwordx4 v146, s[46:47]
	s_mov_b32 m0, s61
	s_nop 0
	global_load_lds_dwordx4 v150, s[46:47]
	ds_read_b128 v[214:217], v161 offset:49152
	ds_read_b128 v[218:221], v161 offset:51200
	ds_read_b128 v[222:225], v162 offset:49152
	ds_read_b128 v[226:229], v162 offset:51200
	s_waitcnt vmcnt(8)
	s_waitcnt lgkmcnt(0)
	s_barrier
	s_waitcnt lgkmcnt(0)
	s_setprio 1
	s_waitcnt lgkmcnt(7)
	v_mfma_f32_16x16x128_f8f6f4 v[18:21], v[166:169], v[182:185], v[18:21] cbsz:4 blgp:4
	s_waitcnt lgkmcnt(5)
	v_mfma_f32_16x16x128_f8f6f4 v[18:21], v[174:177], v[190:193], v[18:21] cbsz:4 blgp:4
	v_mfma_f32_16x16x128_f8f6f4 v[22:25], v[170:173], v[182:185], v[22:25] cbsz:4 blgp:4
	s_nop 0
	v_mfma_f32_16x16x128_f8f6f4 v[22:25], v[178:181], v[190:193], v[22:25] cbsz:4 blgp:4
	v_mfma_f32_16x16x128_f8f6f4 v[26:29], v[166:169], v[186:189], v[26:29] cbsz:4 blgp:4
	s_waitcnt lgkmcnt(4)
	v_mfma_f32_16x16x128_f8f6f4 v[26:29], v[174:177], v[194:197], v[26:29] cbsz:4 blgp:4
	v_mfma_f32_16x16x128_f8f6f4 v[30:33], v[170:173], v[186:189], v[30:33] cbsz:4 blgp:4
	s_nop 0
	v_mfma_f32_16x16x128_f8f6f4 v[30:33], v[178:181], v[194:197], v[30:33] cbsz:4 blgp:4
	s_waitcnt lgkmcnt(3)
	v_mfma_f32_16x16x128_f8f6f4 v[34:37], v[166:169], v[198:201], v[34:37] cbsz:4 blgp:4
	s_waitcnt lgkmcnt(1)
	v_mfma_f32_16x16x128_f8f6f4 v[34:37], v[174:177], v[206:209], v[34:37] cbsz:4 blgp:4
	v_mfma_f32_16x16x128_f8f6f4 v[38:41], v[170:173], v[198:201], v[38:41] cbsz:4 blgp:4
	s_nop 0
	v_mfma_f32_16x16x128_f8f6f4 v[38:41], v[178:181], v[206:209], v[38:41] cbsz:4 blgp:4
	v_mfma_f32_16x16x128_f8f6f4 v[42:45], v[166:169], v[202:205], v[42:45] cbsz:4 blgp:4
	s_waitcnt lgkmcnt(0)
	v_mfma_f32_16x16x128_f8f6f4 v[42:45], v[174:177], v[210:213], v[42:45] cbsz:4 blgp:4
	v_mfma_f32_16x16x128_f8f6f4 v[46:49], v[170:173], v[202:205], v[46:49] cbsz:4 blgp:4
	s_nop 0
	v_mfma_f32_16x16x128_f8f6f4 v[46:49], v[178:181], v[210:213], v[46:49] cbsz:4 blgp:4
	s_waitcnt lgkmcnt(3)
	v_mfma_f32_16x16x128_f8f6f4 v[50:53], v[214:217], v[182:185], v[50:53] cbsz:4 blgp:4
	s_waitcnt lgkmcnt(1)
	v_mfma_f32_16x16x128_f8f6f4 v[50:53], v[222:225], v[190:193], v[50:53] cbsz:4 blgp:4
	v_mfma_f32_16x16x128_f8f6f4 v[54:57], v[218:221], v[182:185], v[54:57] cbsz:4 blgp:4
	s_waitcnt lgkmcnt(0)
	v_mfma_f32_16x16x128_f8f6f4 v[54:57], v[226:229], v[190:193], v[54:57] cbsz:4 blgp:4
	v_mfma_f32_16x16x128_f8f6f4 v[58:61], v[214:217], v[186:189], v[58:61] cbsz:4 blgp:4
	s_nop 0
	v_mfma_f32_16x16x128_f8f6f4 v[58:61], v[222:225], v[194:197], v[58:61] cbsz:4 blgp:4
	v_mfma_f32_16x16x128_f8f6f4 v[62:65], v[218:221], v[186:189], v[62:65] cbsz:4 blgp:4
	s_nop 0
	v_mfma_f32_16x16x128_f8f6f4 v[62:65], v[226:229], v[194:197], v[62:65] cbsz:4 blgp:4
	v_mfma_f32_16x16x128_f8f6f4 v[66:69], v[214:217], v[198:201], v[66:69] cbsz:4 blgp:4
	s_nop 0
	v_mfma_f32_16x16x128_f8f6f4 v[66:69], v[222:225], v[206:209], v[66:69] cbsz:4 blgp:4
	v_mfma_f32_16x16x128_f8f6f4 v[70:73], v[218:221], v[198:201], v[70:73] cbsz:4 blgp:4
	s_nop 0
	v_mfma_f32_16x16x128_f8f6f4 v[70:73], v[226:229], v[206:209], v[70:73] cbsz:4 blgp:4
	v_mfma_f32_16x16x128_f8f6f4 v[74:77], v[214:217], v[202:205], v[74:77] cbsz:4 blgp:4
	s_nop 0
	v_mfma_f32_16x16x128_f8f6f4 v[74:77], v[222:225], v[210:213], v[74:77] cbsz:4 blgp:4
	v_mfma_f32_16x16x128_f8f6f4 v[78:81], v[218:221], v[202:205], v[78:81] cbsz:4 blgp:4
	s_nop 0
	v_mfma_f32_16x16x128_f8f6f4 v[78:81], v[226:229], v[210:213], v[78:81] cbsz:4 blgp:4
	s_setprio 0
	s_barrier
	s_mov_b32 m0, s64
	s_nop 0
	global_load_lds_dwordx4 v148, s[42:43]
	s_mov_b32 m0, s65
	s_nop 0
	global_load_lds_dwordx4 v152, s[42:43]
	ds_read_b128 v[182:185], v163 offset:49152
	ds_read_b128 v[186:189], v163 offset:51200
	ds_read_b128 v[190:193], v164 offset:49152
	ds_read_b128 v[194:197], v164 offset:51200
	ds_read_b128 v[198:201], v163 offset:53248
	ds_read_b128 v[202:205], v163 offset:55296
	ds_read_b128 v[206:209], v164 offset:53248
	ds_read_b128 v[210:213], v164 offset:55296
	s_mov_b32 m0, s66
	s_nop 0
	global_load_lds_dwordx4 v146, s[44:45]
	s_mov_b32 m0, s67
	s_nop 0
	global_load_lds_dwordx4 v150, s[44:45]
	s_add_u32 s42, s42, s24
	s_addc_u32 s43, s43, s25
	s_mov_b32 m0, s68
	s_nop 0
	global_load_lds_dwordx4 v148, s[42:43]
	s_mov_b32 m0, s69
	s_nop 0
	global_load_lds_dwordx4 v152, s[42:43]
	s_waitcnt vmcnt(8)
	s_waitcnt lgkmcnt(0)
	s_barrier
	s_setprio 1
	s_waitcnt lgkmcnt(7)
	v_mfma_f32_16x16x128_f8f6f4 v[86:89], v[166:169], v[182:185], v[86:89] cbsz:4 blgp:4
	s_waitcnt lgkmcnt(5)
	v_mfma_f32_16x16x128_f8f6f4 v[86:89], v[174:177], v[190:193], v[86:89] cbsz:4 blgp:4
	v_mfma_f32_16x16x128_f8f6f4 v[90:93], v[170:173], v[182:185], v[90:93] cbsz:4 blgp:4
	s_nop 0
	v_mfma_f32_16x16x128_f8f6f4 v[90:93], v[178:181], v[190:193], v[90:93] cbsz:4 blgp:4
	v_mfma_f32_16x16x128_f8f6f4 v[98:101], v[166:169], v[186:189], v[98:101] cbsz:4 blgp:4
	s_waitcnt lgkmcnt(4)
	v_mfma_f32_16x16x128_f8f6f4 v[98:101], v[174:177], v[194:197], v[98:101] cbsz:4 blgp:4
	v_mfma_f32_16x16x128_f8f6f4 v[106:109], v[170:173], v[186:189], v[106:109] cbsz:4 blgp:4
	s_nop 0
	v_mfma_f32_16x16x128_f8f6f4 v[106:109], v[178:181], v[194:197], v[106:109] cbsz:4 blgp:4
	s_waitcnt lgkmcnt(3)
	v_mfma_f32_16x16x128_f8f6f4 v[118:121], v[166:169], v[198:201], v[118:121] cbsz:4 blgp:4
	s_waitcnt lgkmcnt(1)
	v_mfma_f32_16x16x128_f8f6f4 v[118:121], v[174:177], v[206:209], v[118:121] cbsz:4 blgp:4
	v_mfma_f32_16x16x128_f8f6f4 v[126:129], v[170:173], v[198:201], v[126:129] cbsz:4 blgp:4
	s_nop 0
	v_mfma_f32_16x16x128_f8f6f4 v[126:129], v[178:181], v[206:209], v[126:129] cbsz:4 blgp:4
	v_mfma_f32_16x16x128_f8f6f4 v[138:141], v[166:169], v[202:205], v[138:141] cbsz:4 blgp:4
	s_waitcnt lgkmcnt(0)
	v_mfma_f32_16x16x128_f8f6f4 v[138:141], v[174:177], v[210:213], v[138:141] cbsz:4 blgp:4
	v_mfma_f32_16x16x128_f8f6f4 v[82:85], v[170:173], v[202:205], v[82:85] cbsz:4 blgp:4
	s_nop 0
	v_mfma_f32_16x16x128_f8f6f4 v[82:85], v[178:181], v[210:213], v[82:85] cbsz:4 blgp:4
	v_mfma_f32_16x16x128_f8f6f4 v[94:97], v[214:217], v[182:185], v[94:97] cbsz:4 blgp:4
	s_nop 0
	v_mfma_f32_16x16x128_f8f6f4 v[94:97], v[222:225], v[190:193], v[94:97] cbsz:4 blgp:4
	v_mfma_f32_16x16x128_f8f6f4 v[102:105], v[218:221], v[182:185], v[102:105] cbsz:4 blgp:4
	s_nop 0
	v_mfma_f32_16x16x128_f8f6f4 v[102:105], v[226:229], v[190:193], v[102:105] cbsz:4 blgp:4
	v_mfma_f32_16x16x128_f8f6f4 v[110:113], v[214:217], v[186:189], v[110:113] cbsz:4 blgp:4
	s_nop 0
	v_mfma_f32_16x16x128_f8f6f4 v[110:113], v[222:225], v[194:197], v[110:113] cbsz:4 blgp:4
	v_mfma_f32_16x16x128_f8f6f4 v[114:117], v[218:221], v[186:189], v[114:117] cbsz:4 blgp:4
	s_nop 0
	v_mfma_f32_16x16x128_f8f6f4 v[114:117], v[226:229], v[194:197], v[114:117] cbsz:4 blgp:4
	v_mfma_f32_16x16x128_f8f6f4 v[122:125], v[214:217], v[198:201], v[122:125] cbsz:4 blgp:4
	s_nop 0
	v_mfma_f32_16x16x128_f8f6f4 v[122:125], v[222:225], v[206:209], v[122:125] cbsz:4 blgp:4
	v_mfma_f32_16x16x128_f8f6f4 v[130:133], v[218:221], v[198:201], v[130:133] cbsz:4 blgp:4
	s_nop 0
	v_mfma_f32_16x16x128_f8f6f4 v[130:133], v[226:229], v[206:209], v[130:133] cbsz:4 blgp:4
	v_mfma_f32_16x16x128_f8f6f4 v[134:137], v[214:217], v[202:205], v[134:137] cbsz:4 blgp:4
	s_nop 0
	v_mfma_f32_16x16x128_f8f6f4 v[134:137], v[222:225], v[210:213], v[134:137] cbsz:4 blgp:4
	v_mfma_f32_16x16x128_f8f6f4 v[142:145], v[218:221], v[202:205], v[142:145] cbsz:4 blgp:4
	s_nop 0
	v_mfma_f32_16x16x128_f8f6f4 v[142:145], v[226:229], v[210:213], v[142:145] cbsz:4 blgp:4
	s_setprio 0
	s_andn2_b64 vcc, exec, s[34:35]
	s_barrier
	s_cbranch_vccnz .LBB4_4
	s_ashr_i32 s29, s28, 31
	s_lshl_b64 s[42:43], s[28:29], 10
	s_add_u32 s42, s10, s42
	s_addc_u32 s43, s11, s43
	s_add_u32 s29, s40, 0x200
	s_addc_u32 s78, s41, 0
	s_add_u32 s79, s38, 0x200
	s_addc_u32 s80, s39, 0
	s_add_u32 s38, s81, 0x180
	s_addc_u32 s39, s82, 0
	s_mov_b32 s81, 4
	s_cmp_eq_u32 s63, s81
	s_cselect_b64 s[40:41], -1, 0
	s_cmp_lg_u32 s63, s81
	s_cbranch_scc1 .LBB4_15

.LBB4_15:
	ds_read_b128 v[166:169], v161
	ds_read_b128 v[170:173], v161 offset:2048
	ds_read_b128 v[174:177], v162
	ds_read_b128 v[178:181], v162 offset:2048
	s_and_b64 s[40:41], s[40:41], exec
	s_cselect_b32 s46, s36, s29
	s_cselect_b32 s47, s37, s78
	s_cselect_b32 s49, s5, s80
	s_cselect_b32 s48, s4, s79
	s_add_u32 s44, s46, 0x80
	s_addc_u32 s45, s47, 0
	s_add_u32 s40, s48, 0x80
	s_addc_u32 s41, s49, 0
	ds_read_b128 v[182:185], v163
	ds_read_b128 v[186:189], v163 offset:2048
	ds_read_b128 v[190:193], v164
	ds_read_b128 v[194:197], v164 offset:2048
	ds_read_b128 v[198:201], v163 offset:4096
	ds_read_b128 v[202:205], v163 offset:6144
	ds_read_b128 v[206:209], v164 offset:4096
	ds_read_b128 v[210:213], v164 offset:6144
	s_mov_b32 m0, s70
	s_nop 0
	global_load_lds_dwordx4 v146, s[38:39]
	s_mov_b32 m0, s71
	s_nop 0
	global_load_lds_dwordx4 v150, s[38:39]
	ds_read_b128 v[214:217], v161 offset:16384
	ds_read_b128 v[218:221], v161 offset:18432
	ds_read_b128 v[222:225], v162 offset:16384
	ds_read_b128 v[226:229], v162 offset:18432
	s_waitcnt vmcnt(8)
	s_waitcnt lgkmcnt(0)
	s_barrier
	s_waitcnt lgkmcnt(0)
	s_setprio 1
	s_waitcnt lgkmcnt(7)
	v_mfma_f32_16x16x128_f8f6f4 v[18:21], v[166:169], v[182:185], v[18:21] cbsz:4 blgp:4
	s_waitcnt lgkmcnt(5)
	v_mfma_f32_16x16x128_f8f6f4 v[18:21], v[174:177], v[190:193], v[18:21] cbsz:4 blgp:4
	v_mfma_f32_16x16x128_f8f6f4 v[22:25], v[170:173], v[182:185], v[22:25] cbsz:4 blgp:4
	s_nop 0
	v_mfma_f32_16x16x128_f8f6f4 v[22:25], v[178:181], v[190:193], v[22:25] cbsz:4 blgp:4
	v_mfma_f32_16x16x128_f8f6f4 v[26:29], v[166:169], v[186:189], v[26:29] cbsz:4 blgp:4
	s_waitcnt lgkmcnt(4)
	v_mfma_f32_16x16x128_f8f6f4 v[26:29], v[174:177], v[194:197], v[26:29] cbsz:4 blgp:4
	v_mfma_f32_16x16x128_f8f6f4 v[30:33], v[170:173], v[186:189], v[30:33] cbsz:4 blgp:4
	s_nop 0
	v_mfma_f32_16x16x128_f8f6f4 v[30:33], v[178:181], v[194:197], v[30:33] cbsz:4 blgp:4
	s_waitcnt lgkmcnt(3)
	v_mfma_f32_16x16x128_f8f6f4 v[34:37], v[166:169], v[198:201], v[34:37] cbsz:4 blgp:4
	s_waitcnt lgkmcnt(1)
	v_mfma_f32_16x16x128_f8f6f4 v[34:37], v[174:177], v[206:209], v[34:37] cbsz:4 blgp:4
	v_mfma_f32_16x16x128_f8f6f4 v[38:41], v[170:173], v[198:201], v[38:41] cbsz:4 blgp:4
	s_nop 0
	v_mfma_f32_16x16x128_f8f6f4 v[38:41], v[178:181], v[206:209], v[38:41] cbsz:4 blgp:4
	v_mfma_f32_16x16x128_f8f6f4 v[42:45], v[166:169], v[202:205], v[42:45] cbsz:4 blgp:4
	s_waitcnt lgkmcnt(0)
	v_mfma_f32_16x16x128_f8f6f4 v[42:45], v[174:177], v[210:213], v[42:45] cbsz:4 blgp:4
	v_mfma_f32_16x16x128_f8f6f4 v[46:49], v[170:173], v[202:205], v[46:49] cbsz:4 blgp:4
	s_nop 0
	v_mfma_f32_16x16x128_f8f6f4 v[46:49], v[178:181], v[210:213], v[46:49] cbsz:4 blgp:4
	s_waitcnt lgkmcnt(3)
	v_mfma_f32_16x16x128_f8f6f4 v[50:53], v[214:217], v[182:185], v[50:53] cbsz:4 blgp:4
	s_waitcnt lgkmcnt(1)
	v_mfma_f32_16x16x128_f8f6f4 v[50:53], v[222:225], v[190:193], v[50:53] cbsz:4 blgp:4
	v_mfma_f32_16x16x128_f8f6f4 v[54:57], v[218:221], v[182:185], v[54:57] cbsz:4 blgp:4
	s_waitcnt lgkmcnt(0)
	v_mfma_f32_16x16x128_f8f6f4 v[54:57], v[226:229], v[190:193], v[54:57] cbsz:4 blgp:4
	v_mfma_f32_16x16x128_f8f6f4 v[58:61], v[214:217], v[186:189], v[58:61] cbsz:4 blgp:4
	s_nop 0
	v_mfma_f32_16x16x128_f8f6f4 v[58:61], v[222:225], v[194:197], v[58:61] cbsz:4 blgp:4
	v_mfma_f32_16x16x128_f8f6f4 v[62:65], v[218:221], v[186:189], v[62:65] cbsz:4 blgp:4
	s_nop 0
	v_mfma_f32_16x16x128_f8f6f4 v[62:65], v[226:229], v[194:197], v[62:65] cbsz:4 blgp:4
	v_mfma_f32_16x16x128_f8f6f4 v[66:69], v[214:217], v[198:201], v[66:69] cbsz:4 blgp:4
	s_nop 0
	v_mfma_f32_16x16x128_f8f6f4 v[66:69], v[222:225], v[206:209], v[66:69] cbsz:4 blgp:4
	v_mfma_f32_16x16x128_f8f6f4 v[70:73], v[218:221], v[198:201], v[70:73] cbsz:4 blgp:4
	s_nop 0
	v_mfma_f32_16x16x128_f8f6f4 v[70:73], v[226:229], v[206:209], v[70:73] cbsz:4 blgp:4
	v_mfma_f32_16x16x128_f8f6f4 v[74:77], v[214:217], v[202:205], v[74:77] cbsz:4 blgp:4
	s_nop 0
	v_mfma_f32_16x16x128_f8f6f4 v[74:77], v[222:225], v[210:213], v[74:77] cbsz:4 blgp:4
	v_mfma_f32_16x16x128_f8f6f4 v[78:81], v[218:221], v[202:205], v[78:81] cbsz:4 blgp:4
	s_nop 0
	v_mfma_f32_16x16x128_f8f6f4 v[78:81], v[226:229], v[210:213], v[78:81] cbsz:4 blgp:4
	s_setprio 0
	s_barrier
	s_mov_b32 m0, s55
	s_nop 0
	global_load_lds_dwordx4 v148, s[48:49]
	s_mov_b32 m0, s56
	s_nop 0
	global_load_lds_dwordx4 v152, s[48:49]
	ds_read_b128 v[182:185], v163 offset:16384
	ds_read_b128 v[186:189], v163 offset:18432
	ds_read_b128 v[190:193], v164 offset:16384
	ds_read_b128 v[194:197], v164 offset:18432
	ds_read_b128 v[198:201], v163 offset:20480
	ds_read_b128 v[202:205], v163 offset:22528
	ds_read_b128 v[206:209], v164 offset:20480
	ds_read_b128 v[210:213], v164 offset:22528
	s_mov_b32 m0, s54
	s_nop 0
	global_load_lds_dwordx4 v146, s[46:47]
	s_mov_b32 m0, s57
	s_nop 0
	global_load_lds_dwordx4 v150, s[46:47]
	s_add_u32 s48, s48, s24
	s_addc_u32 s49, s49, s25
	s_mov_b32 m0, s58
	s_nop 0
	global_load_lds_dwordx4 v148, s[48:49]
	s_mov_b32 m0, s59
	s_nop 0
	global_load_lds_dwordx4 v152, s[48:49]
	s_waitcnt vmcnt(8)
	s_waitcnt lgkmcnt(0)
	s_barrier
	s_setprio 1
	s_waitcnt lgkmcnt(7)
	v_mfma_f32_16x16x128_f8f6f4 v[86:89], v[166:169], v[182:185], v[86:89] cbsz:4 blgp:4
	s_waitcnt lgkmcnt(5)
	v_mfma_f32_16x16x128_f8f6f4 v[86:89], v[174:177], v[190:193], v[86:89] cbsz:4 blgp:4
	v_mfma_f32_16x16x128_f8f6f4 v[90:93], v[170:173], v[182:185], v[90:93] cbsz:4 blgp:4
	s_nop 0
	v_mfma_f32_16x16x128_f8f6f4 v[90:93], v[178:181], v[190:193], v[90:93] cbsz:4 blgp:4
	v_mfma_f32_16x16x128_f8f6f4 v[98:101], v[166:169], v[186:189], v[98:101] cbsz:4 blgp:4
	s_waitcnt lgkmcnt(4)
	v_mfma_f32_16x16x128_f8f6f4 v[98:101], v[174:177], v[194:197], v[98:101] cbsz:4 blgp:4
	v_mfma_f32_16x16x128_f8f6f4 v[106:109], v[170:173], v[186:189], v[106:109] cbsz:4 blgp:4
	s_nop 0
	v_mfma_f32_16x16x128_f8f6f4 v[106:109], v[178:181], v[194:197], v[106:109] cbsz:4 blgp:4
	s_waitcnt lgkmcnt(3)
	v_mfma_f32_16x16x128_f8f6f4 v[118:121], v[166:169], v[198:201], v[118:121] cbsz:4 blgp:4
	s_waitcnt lgkmcnt(1)
	v_mfma_f32_16x16x128_f8f6f4 v[118:121], v[174:177], v[206:209], v[118:121] cbsz:4 blgp:4
	v_mfma_f32_16x16x128_f8f6f4 v[126:129], v[170:173], v[198:201], v[126:129] cbsz:4 blgp:4
	s_nop 0
	v_mfma_f32_16x16x128_f8f6f4 v[126:129], v[178:181], v[206:209], v[126:129] cbsz:4 blgp:4
	v_mfma_f32_16x16x128_f8f6f4 v[138:141], v[166:169], v[202:205], v[138:141] cbsz:4 blgp:4
	s_waitcnt lgkmcnt(0)
	v_mfma_f32_16x16x128_f8f6f4 v[138:141], v[174:177], v[210:213], v[138:141] cbsz:4 blgp:4
	v_mfma_f32_16x16x128_f8f6f4 v[82:85], v[170:173], v[202:205], v[82:85] cbsz:4 blgp:4
	s_nop 0
	v_mfma_f32_16x16x128_f8f6f4 v[82:85], v[178:181], v[210:213], v[82:85] cbsz:4 blgp:4
	v_mfma_f32_16x16x128_f8f6f4 v[94:97], v[214:217], v[182:185], v[94:97] cbsz:4 blgp:4
	s_nop 0
	v_mfma_f32_16x16x128_f8f6f4 v[94:97], v[222:225], v[190:193], v[94:97] cbsz:4 blgp:4
	v_mfma_f32_16x16x128_f8f6f4 v[102:105], v[218:221], v[182:185], v[102:105] cbsz:4 blgp:4
	s_nop 0
	v_mfma_f32_16x16x128_f8f6f4 v[102:105], v[226:229], v[190:193], v[102:105] cbsz:4 blgp:4
	v_mfma_f32_16x16x128_f8f6f4 v[110:113], v[214:217], v[186:189], v[110:113] cbsz:4 blgp:4
	s_nop 0
	v_mfma_f32_16x16x128_f8f6f4 v[110:113], v[222:225], v[194:197], v[110:113] cbsz:4 blgp:4
	v_mfma_f32_16x16x128_f8f6f4 v[114:117], v[218:221], v[186:189], v[114:117] cbsz:4 blgp:4
	s_nop 0
	v_mfma_f32_16x16x128_f8f6f4 v[114:117], v[226:229], v[194:197], v[114:117] cbsz:4 blgp:4
	v_mfma_f32_16x16x128_f8f6f4 v[122:125], v[214:217], v[198:201], v[122:125] cbsz:4 blgp:4
	s_nop 0
	v_mfma_f32_16x16x128_f8f6f4 v[122:125], v[222:225], v[206:209], v[122:125] cbsz:4 blgp:4
	v_mfma_f32_16x16x128_f8f6f4 v[130:133], v[218:221], v[198:201], v[130:133] cbsz:4 blgp:4
	s_nop 0
	v_mfma_f32_16x16x128_f8f6f4 v[130:133], v[226:229], v[206:209], v[130:133] cbsz:4 blgp:4
	v_mfma_f32_16x16x128_f8f6f4 v[134:137], v[214:217], v[202:205], v[134:137] cbsz:4 blgp:4
	s_nop 0
	v_mfma_f32_16x16x128_f8f6f4 v[134:137], v[222:225], v[210:213], v[134:137] cbsz:4 blgp:4
	v_mfma_f32_16x16x128_f8f6f4 v[142:145], v[218:221], v[202:205], v[142:145] cbsz:4 blgp:4
	s_nop 0
	v_mfma_f32_16x16x128_f8f6f4 v[142:145], v[226:229], v[210:213], v[142:145] cbsz:4 blgp:4
	s_setprio 0
	s_barrier
	ds_read_b128 v[166:169], v161 offset:32768
	ds_read_b128 v[170:173], v161 offset:34816
	ds_read_b128 v[174:177], v162 offset:32768
	ds_read_b128 v[178:181], v162 offset:34816
	ds_read_b128 v[182:185], v163 offset:32768
	ds_read_b128 v[186:189], v163 offset:34816
	ds_read_b128 v[190:193], v164 offset:32768
	ds_read_b128 v[194:197], v164 offset:34816
	ds_read_b128 v[198:201], v163 offset:36864
	ds_read_b128 v[202:205], v163 offset:38912
	ds_read_b128 v[206:209], v164 offset:36864
	ds_read_b128 v[210:213], v164 offset:38912
	s_add_u32 s46, s46, s22
	s_addc_u32 s47, s47, s23
	s_mov_b32 m0, s60
	s_nop 0
	global_load_lds_dwordx4 v146, s[46:47]
	s_mov_b32 m0, s61
	s_nop 0
	global_load_lds_dwordx4 v150, s[46:47]
	ds_read_b128 v[214:217], v161 offset:49152
	ds_read_b128 v[218:221], v161 offset:51200
	ds_read_b128 v[222:225], v162 offset:49152
	ds_read_b128 v[226:229], v162 offset:51200
	s_waitcnt vmcnt(8)
	s_waitcnt lgkmcnt(0)
	s_barrier
	s_waitcnt lgkmcnt(0)
	s_setprio 1
	s_waitcnt lgkmcnt(7)
	v_mfma_f32_16x16x128_f8f6f4 v[18:21], v[166:169], v[182:185], v[18:21] cbsz:4 blgp:4
	s_waitcnt lgkmcnt(5)
	v_mfma_f32_16x16x128_f8f6f4 v[18:21], v[174:177], v[190:193], v[18:21] cbsz:4 blgp:4
	v_mfma_f32_16x16x128_f8f6f4 v[22:25], v[170:173], v[182:185], v[22:25] cbsz:4 blgp:4
	s_nop 0
	v_mfma_f32_16x16x128_f8f6f4 v[22:25], v[178:181], v[190:193], v[22:25] cbsz:4 blgp:4
	v_mfma_f32_16x16x128_f8f6f4 v[26:29], v[166:169], v[186:189], v[26:29] cbsz:4 blgp:4
	s_waitcnt lgkmcnt(4)
	v_mfma_f32_16x16x128_f8f6f4 v[26:29], v[174:177], v[194:197], v[26:29] cbsz:4 blgp:4
	v_mfma_f32_16x16x128_f8f6f4 v[30:33], v[170:173], v[186:189], v[30:33] cbsz:4 blgp:4
	s_nop 0
	v_mfma_f32_16x16x128_f8f6f4 v[30:33], v[178:181], v[194:197], v[30:33] cbsz:4 blgp:4
	s_waitcnt lgkmcnt(3)
	v_mfma_f32_16x16x128_f8f6f4 v[34:37], v[166:169], v[198:201], v[34:37] cbsz:4 blgp:4
	s_waitcnt lgkmcnt(1)
	v_mfma_f32_16x16x128_f8f6f4 v[34:37], v[174:177], v[206:209], v[34:37] cbsz:4 blgp:4
	v_mfma_f32_16x16x128_f8f6f4 v[38:41], v[170:173], v[198:201], v[38:41] cbsz:4 blgp:4
	s_nop 0
	v_mfma_f32_16x16x128_f8f6f4 v[38:41], v[178:181], v[206:209], v[38:41] cbsz:4 blgp:4
	v_mfma_f32_16x16x128_f8f6f4 v[42:45], v[166:169], v[202:205], v[42:45] cbsz:4 blgp:4
	s_waitcnt lgkmcnt(0)
	v_mfma_f32_16x16x128_f8f6f4 v[42:45], v[174:177], v[210:213], v[42:45] cbsz:4 blgp:4
	v_mfma_f32_16x16x128_f8f6f4 v[46:49], v[170:173], v[202:205], v[46:49] cbsz:4 blgp:4
	s_nop 0
	v_mfma_f32_16x16x128_f8f6f4 v[46:49], v[178:181], v[210:213], v[46:49] cbsz:4 blgp:4
	s_waitcnt lgkmcnt(3)
	v_mfma_f32_16x16x128_f8f6f4 v[50:53], v[214:217], v[182:185], v[50:53] cbsz:4 blgp:4
	s_waitcnt lgkmcnt(1)
	v_mfma_f32_16x16x128_f8f6f4 v[50:53], v[222:225], v[190:193], v[50:53] cbsz:4 blgp:4
	v_mfma_f32_16x16x128_f8f6f4 v[54:57], v[218:221], v[182:185], v[54:57] cbsz:4 blgp:4
	s_waitcnt lgkmcnt(0)
	v_mfma_f32_16x16x128_f8f6f4 v[54:57], v[226:229], v[190:193], v[54:57] cbsz:4 blgp:4
	v_mfma_f32_16x16x128_f8f6f4 v[58:61], v[214:217], v[186:189], v[58:61] cbsz:4 blgp:4
	s_nop 0
	v_mfma_f32_16x16x128_f8f6f4 v[58:61], v[222:225], v[194:197], v[58:61] cbsz:4 blgp:4
	v_mfma_f32_16x16x128_f8f6f4 v[62:65], v[218:221], v[186:189], v[62:65] cbsz:4 blgp:4
	s_nop 0
	v_mfma_f32_16x16x128_f8f6f4 v[62:65], v[226:229], v[194:197], v[62:65] cbsz:4 blgp:4
	v_mfma_f32_16x16x128_f8f6f4 v[66:69], v[214:217], v[198:201], v[66:69] cbsz:4 blgp:4
	s_nop 0
	v_mfma_f32_16x16x128_f8f6f4 v[66:69], v[222:225], v[206:209], v[66:69] cbsz:4 blgp:4
	v_mfma_f32_16x16x128_f8f6f4 v[70:73], v[218:221], v[198:201], v[70:73] cbsz:4 blgp:4
	s_nop 0
	v_mfma_f32_16x16x128_f8f6f4 v[70:73], v[226:229], v[206:209], v[70:73] cbsz:4 blgp:4
	v_mfma_f32_16x16x128_f8f6f4 v[74:77], v[214:217], v[202:205], v[74:77] cbsz:4 blgp:4
	s_nop 0
	v_mfma_f32_16x16x128_f8f6f4 v[74:77], v[222:225], v[210:213], v[74:77] cbsz:4 blgp:4
	v_mfma_f32_16x16x128_f8f6f4 v[78:81], v[218:221], v[202:205], v[78:81] cbsz:4 blgp:4
	s_nop 0
	v_mfma_f32_16x16x128_f8f6f4 v[78:81], v[226:229], v[210:213], v[78:81] cbsz:4 blgp:4
	s_setprio 0
	s_barrier
	s_mov_b32 m0, s64
	s_nop 0
	global_load_lds_dwordx4 v148, s[40:41]
	s_mov_b32 m0, s65
	s_nop 0
	global_load_lds_dwordx4 v152, s[40:41]
	ds_read_b128 v[182:185], v163 offset:49152
	ds_read_b128 v[186:189], v163 offset:51200
	ds_read_b128 v[190:193], v164 offset:49152
	ds_read_b128 v[194:197], v164 offset:51200
	ds_read_b128 v[198:201], v163 offset:53248
	ds_read_b128 v[202:205], v163 offset:55296
	ds_read_b128 v[206:209], v164 offset:53248
	ds_read_b128 v[210:213], v164 offset:55296
	s_mov_b32 m0, s66
	s_nop 0
	global_load_lds_dwordx4 v146, s[44:45]
	s_mov_b32 m0, s67
	s_nop 0
	global_load_lds_dwordx4 v150, s[44:45]
	s_add_u32 s40, s40, s24
	s_addc_u32 s41, s41, s25
	s_mov_b32 m0, s68
	s_nop 0
	global_load_lds_dwordx4 v148, s[40:41]
	s_mov_b32 m0, s69
	s_nop 0
	global_load_lds_dwordx4 v152, s[40:41]
	s_waitcnt vmcnt(8)
	s_waitcnt lgkmcnt(0)
	s_barrier
	s_setprio 1
	s_waitcnt lgkmcnt(7)
	v_mfma_f32_16x16x128_f8f6f4 v[86:89], v[166:169], v[182:185], v[86:89] cbsz:4 blgp:4
	s_waitcnt lgkmcnt(5)
	v_mfma_f32_16x16x128_f8f6f4 v[86:89], v[174:177], v[190:193], v[86:89] cbsz:4 blgp:4
	v_mfma_f32_16x16x128_f8f6f4 v[90:93], v[170:173], v[182:185], v[90:93] cbsz:4 blgp:4
	s_nop 0
	v_mfma_f32_16x16x128_f8f6f4 v[90:93], v[178:181], v[190:193], v[90:93] cbsz:4 blgp:4
	v_mfma_f32_16x16x128_f8f6f4 v[98:101], v[166:169], v[186:189], v[98:101] cbsz:4 blgp:4
	s_waitcnt lgkmcnt(4)
	v_mfma_f32_16x16x128_f8f6f4 v[98:101], v[174:177], v[194:197], v[98:101] cbsz:4 blgp:4
	v_mfma_f32_16x16x128_f8f6f4 v[106:109], v[170:173], v[186:189], v[106:109] cbsz:4 blgp:4
	s_nop 0
	v_mfma_f32_16x16x128_f8f6f4 v[106:109], v[178:181], v[194:197], v[106:109] cbsz:4 blgp:4
	s_waitcnt lgkmcnt(3)
	v_mfma_f32_16x16x128_f8f6f4 v[118:121], v[166:169], v[198:201], v[118:121] cbsz:4 blgp:4
	s_waitcnt lgkmcnt(1)
	v_mfma_f32_16x16x128_f8f6f4 v[118:121], v[174:177], v[206:209], v[118:121] cbsz:4 blgp:4
	v_mfma_f32_16x16x128_f8f6f4 v[126:129], v[170:173], v[198:201], v[126:129] cbsz:4 blgp:4
	s_nop 0
	v_mfma_f32_16x16x128_f8f6f4 v[126:129], v[178:181], v[206:209], v[126:129] cbsz:4 blgp:4
	v_mfma_f32_16x16x128_f8f6f4 v[138:141], v[166:169], v[202:205], v[138:141] cbsz:4 blgp:4
	s_waitcnt lgkmcnt(0)
	v_mfma_f32_16x16x128_f8f6f4 v[138:141], v[174:177], v[210:213], v[138:141] cbsz:4 blgp:4
	v_mfma_f32_16x16x128_f8f6f4 v[82:85], v[170:173], v[202:205], v[82:85] cbsz:4 blgp:4
	s_nop 0
	v_mfma_f32_16x16x128_f8f6f4 v[82:85], v[178:181], v[210:213], v[82:85] cbsz:4 blgp:4
	v_mfma_f32_16x16x128_f8f6f4 v[94:97], v[214:217], v[182:185], v[94:97] cbsz:4 blgp:4
	s_nop 0
	v_mfma_f32_16x16x128_f8f6f4 v[94:97], v[222:225], v[190:193], v[94:97] cbsz:4 blgp:4
	v_mfma_f32_16x16x128_f8f6f4 v[102:105], v[218:221], v[182:185], v[102:105] cbsz:4 blgp:4
	s_nop 0
	v_mfma_f32_16x16x128_f8f6f4 v[102:105], v[226:229], v[190:193], v[102:105] cbsz:4 blgp:4
	v_mfma_f32_16x16x128_f8f6f4 v[110:113], v[214:217], v[186:189], v[110:113] cbsz:4 blgp:4
	s_nop 0
	v_mfma_f32_16x16x128_f8f6f4 v[110:113], v[222:225], v[194:197], v[110:113] cbsz:4 blgp:4
	v_mfma_f32_16x16x128_f8f6f4 v[114:117], v[218:221], v[186:189], v[114:117] cbsz:4 blgp:4
	s_nop 0
	v_mfma_f32_16x16x128_f8f6f4 v[114:117], v[226:229], v[194:197], v[114:117] cbsz:4 blgp:4
	v_mfma_f32_16x16x128_f8f6f4 v[122:125], v[214:217], v[198:201], v[122:125] cbsz:4 blgp:4
	s_nop 0
	v_mfma_f32_16x16x128_f8f6f4 v[122:125], v[222:225], v[206:209], v[122:125] cbsz:4 blgp:4
	v_mfma_f32_16x16x128_f8f6f4 v[130:133], v[218:221], v[198:201], v[130:133] cbsz:4 blgp:4
	s_nop 0
	v_mfma_f32_16x16x128_f8f6f4 v[130:133], v[226:229], v[206:209], v[130:133] cbsz:4 blgp:4
	v_mfma_f32_16x16x128_f8f6f4 v[134:137], v[214:217], v[202:205], v[134:137] cbsz:4 blgp:4
	s_nop 0
	v_mfma_f32_16x16x128_f8f6f4 v[134:137], v[222:225], v[210:213], v[134:137] cbsz:4 blgp:4
	v_mfma_f32_16x16x128_f8f6f4 v[142:145], v[218:221], v[202:205], v[142:145] cbsz:4 blgp:4
	s_nop 0
	v_mfma_f32_16x16x128_f8f6f4 v[142:145], v[226:229], v[210:213], v[142:145] cbsz:4 blgp:4
	s_setprio 0
	s_add_i32 s40, s81, 2
	s_add_u32 s29, s29, 0x100
	s_addc_u32 s78, s78, 0
	s_add_u32 s79, s79, 0x100
	s_addc_u32 s80, s80, 0
	s_add_u32 s38, s38, 0x100
	s_addc_u32 s39, s39, 0
	s_cmp_ge_i32 s81, s63
	s_barrier
	s_cbranch_scc1 .LBB4_4
	s_mov_b32 s81, s40
	s_cmp_eq_u32 s63, s81
	s_cselect_b64 s[40:41], -1, 0
	s_cmp_lg_u32 s63, s81
	s_cbranch_scc0 .LBB4_14
	s_branch .LBB4_15

.LBB5_12:
	s_add_u32 s82, s42, s22
	s_addc_u32 s83, s43, s23
	s_add_u32 s29, s42, 0x100
	s_addc_u32 s46, s43, 0
	s_and_b64 s[44:45], s[14:15], exec
	ds_read_b128 v[82:85], v163
	ds_read_b128 v[94:97], v163 offset:2048
	ds_read_b128 v[102:105], v164
	ds_read_b128 v[110:113], v164 offset:2048
	s_cselect_b32 s49, s39, s46
	s_cselect_b32 s48, s38, s29
	s_add_u32 s29, s40, 0x100
	s_addc_u32 s46, s41, 0
	s_and_b64 s[44:45], s[14:15], exec
	s_cselect_b32 s51, s5, s46
	s_cselect_b32 s50, s4, s29
	s_add_u32 s46, s48, 0x80
	s_addc_u32 s47, s49, 0
	s_add_u32 s44, s50, 0x80
	s_addc_u32 s45, s51, 0
	ds_read_b128 v[58:61], v165
	ds_read_b128 v[66:69], v165 offset:2048
	ds_read_b128 v[62:65], v166
	ds_read_b128 v[70:73], v166 offset:2048
	ds_read_b128 v[74:77], v165 offset:4096
	ds_read_b128 v[86:89], v165 offset:6144
	ds_read_b128 v[78:81], v166 offset:4096
	ds_read_b128 v[90:93], v166 offset:6144
	s_add_u32 s80, s82, 0x80
	s_addc_u32 s81, s83, 0
	s_mov_b32 m0, s71
	s_nop 0
	global_load_lds_dwordx4 v146, s[80:81]
	s_mov_b32 m0, s72
	s_nop 0
	global_load_lds_dwordx4 v150, s[80:81]
	ds_read_b128 v[142:145], v163 offset:16384
	ds_read_b128 v[156:159], v163 offset:18432
	ds_read_b128 v[168:171], v164 offset:16384
	ds_read_b128 v[172:175], v164 offset:18432
	s_waitcnt vmcnt(8)
	s_waitcnt lgkmcnt(0)
	s_barrier
	s_waitcnt lgkmcnt(0)
	s_waitcnt vmcnt(16)
	v_mov_b32_e32 v1, v0
	v_pk_mul_f32 v[16:17], v[0:1], v[16:17]
	v_pk_mul_f32 v[14:15], v[154:155], v[14:15]
	v_pk_mul_f32 v[12:13], v[0:1], v[12:13]
	v_pk_mul_f32 v[10:11], v[154:155], v[10:11]
	v_pk_mul_f32 v[8:9], v[0:1], v[8:9]
	v_pk_mul_f32 v[6:7], v[154:155], v[6:7]
	v_pk_mul_f32 v[4:5], v[0:1], v[4:5]
	v_pk_mul_f32 v[2:3], v[154:155], v[2:3]
	s_setprio 1
	s_waitcnt lgkmcnt(7)
	v_mfma_f32_16x16x128_f8f6f4 v[18:21], v[82:85], v[58:61], v[14:17] cbsz:4 blgp:4
	s_waitcnt lgkmcnt(5)
	v_mfma_f32_16x16x128_f8f6f4 v[18:21], v[102:105], v[62:65], v[18:21] cbsz:4 blgp:4
	v_mfma_f32_16x16x128_f8f6f4 v[22:25], v[94:97], v[58:61], v[10:13] cbsz:4 blgp:4
	s_nop 0
	v_mfma_f32_16x16x128_f8f6f4 v[22:25], v[110:113], v[62:65], v[22:25] cbsz:4 blgp:4
	v_mfma_f32_16x16x128_f8f6f4 v[26:29], v[82:85], v[66:69], v[14:17] cbsz:4 blgp:4
	s_waitcnt lgkmcnt(4)
	v_mfma_f32_16x16x128_f8f6f4 v[26:29], v[102:105], v[70:73], v[26:29] cbsz:4 blgp:4
	v_mfma_f32_16x16x128_f8f6f4 v[30:33], v[94:97], v[66:69], v[10:13] cbsz:4 blgp:4
	s_nop 0
	v_mfma_f32_16x16x128_f8f6f4 v[30:33], v[110:113], v[70:73], v[30:33] cbsz:4 blgp:4
	s_waitcnt lgkmcnt(3)
	v_mfma_f32_16x16x128_f8f6f4 v[34:37], v[82:85], v[74:77], v[14:17] cbsz:4 blgp:4
	s_waitcnt lgkmcnt(1)
	v_mfma_f32_16x16x128_f8f6f4 v[34:37], v[102:105], v[78:81], v[34:37] cbsz:4 blgp:4
	v_mfma_f32_16x16x128_f8f6f4 v[38:41], v[94:97], v[74:77], v[10:13] cbsz:4 blgp:4
	s_nop 0
	v_mfma_f32_16x16x128_f8f6f4 v[38:41], v[110:113], v[78:81], v[38:41] cbsz:4 blgp:4
	v_mfma_f32_16x16x128_f8f6f4 v[42:45], v[82:85], v[86:89], v[14:17] cbsz:4 blgp:4
	s_waitcnt lgkmcnt(0)
	v_mfma_f32_16x16x128_f8f6f4 v[42:45], v[102:105], v[90:93], v[42:45] cbsz:4 blgp:4
	v_mfma_f32_16x16x128_f8f6f4 v[46:49], v[94:97], v[86:89], v[10:13] cbsz:4 blgp:4
	s_nop 0
	v_mfma_f32_16x16x128_f8f6f4 v[46:49], v[110:113], v[90:93], v[46:49] cbsz:4 blgp:4
	s_waitcnt lgkmcnt(3)
	v_mfma_f32_16x16x128_f8f6f4 v[50:53], v[142:145], v[58:61], v[6:9] cbsz:4 blgp:4
	s_waitcnt lgkmcnt(1)
	v_mfma_f32_16x16x128_f8f6f4 v[50:53], v[168:171], v[62:65], v[50:53] cbsz:4 blgp:4
	v_mfma_f32_16x16x128_f8f6f4 v[54:57], v[156:159], v[58:61], v[2:5] cbsz:4 blgp:4
	s_waitcnt lgkmcnt(0)
	v_mfma_f32_16x16x128_f8f6f4 v[54:57], v[172:175], v[62:65], v[54:57] cbsz:4 blgp:4
	v_mfma_f32_16x16x128_f8f6f4 v[58:61], v[142:145], v[66:69], v[6:9] cbsz:4 blgp:4
	s_nop 0
	v_mfma_f32_16x16x128_f8f6f4 v[58:61], v[168:171], v[70:73], v[58:61] cbsz:4 blgp:4
	v_mfma_f32_16x16x128_f8f6f4 v[62:65], v[156:159], v[66:69], v[2:5] cbsz:4 blgp:4
	s_nop 0
	v_mfma_f32_16x16x128_f8f6f4 v[62:65], v[172:175], v[70:73], v[62:65] cbsz:4 blgp:4
	v_mfma_f32_16x16x128_f8f6f4 v[66:69], v[142:145], v[74:77], v[6:9] cbsz:4 blgp:4
	s_nop 0
	v_mfma_f32_16x16x128_f8f6f4 v[66:69], v[168:171], v[78:81], v[66:69] cbsz:4 blgp:4
	v_mfma_f32_16x16x128_f8f6f4 v[70:73], v[156:159], v[74:77], v[2:5] cbsz:4 blgp:4
	s_nop 0
	v_mfma_f32_16x16x128_f8f6f4 v[70:73], v[172:175], v[78:81], v[70:73] cbsz:4 blgp:4
	v_mfma_f32_16x16x128_f8f6f4 v[74:77], v[142:145], v[86:89], v[6:9] cbsz:4 blgp:4
	s_nop 0
	v_mfma_f32_16x16x128_f8f6f4 v[74:77], v[168:171], v[90:93], v[74:77] cbsz:4 blgp:4
	v_mfma_f32_16x16x128_f8f6f4 v[78:81], v[156:159], v[86:89], v[2:5] cbsz:4 blgp:4
	s_nop 0
	v_mfma_f32_16x16x128_f8f6f4 v[78:81], v[172:175], v[90:93], v[78:81] cbsz:4 blgp:4
	s_setprio 0
	s_barrier
	s_mov_b32 m0, s56
	s_nop 0
	global_load_lds_dwordx4 v148, s[50:51]
	s_mov_b32 m0, s57
	s_nop 0
	global_load_lds_dwordx4 v152, s[50:51]
	ds_read_b128 v[114:117], v165 offset:16384
	ds_read_b128 v[122:125], v165 offset:18432
	ds_read_b128 v[130:133], v166 offset:16384
	ds_read_b128 v[134:137], v166 offset:18432
	ds_read_b128 v[176:179], v165 offset:20480
	ds_read_b128 v[180:183], v165 offset:22528
	ds_read_b128 v[184:187], v166 offset:20480
	ds_read_b128 v[188:191], v166 offset:22528
	s_mov_b32 m0, s55
	s_nop 0
	global_load_lds_dwordx4 v146, s[48:49]
	s_mov_b32 m0, s58
	s_nop 0
	global_load_lds_dwordx4 v150, s[48:49]
	s_add_u32 s50, s50, s24
	s_addc_u32 s51, s51, s25
	s_mov_b32 m0, s59
	s_nop 0
	global_load_lds_dwordx4 v148, s[50:51]
	s_mov_b32 m0, s60
	s_nop 0
	global_load_lds_dwordx4 v152, s[50:51]
	s_waitcnt vmcnt(8)
	s_waitcnt lgkmcnt(0)
	s_barrier
	s_setprio 1
	s_waitcnt lgkmcnt(7)
	v_mfma_f32_16x16x128_f8f6f4 v[86:89], v[82:85], v[114:117], v[14:17] cbsz:4 blgp:4
	s_waitcnt lgkmcnt(5)
	v_mfma_f32_16x16x128_f8f6f4 v[86:89], v[102:105], v[130:133], v[86:89] cbsz:4 blgp:4
	v_mfma_f32_16x16x128_f8f6f4 v[90:93], v[94:97], v[114:117], v[10:13] cbsz:4 blgp:4
	s_nop 0
	v_mfma_f32_16x16x128_f8f6f4 v[90:93], v[110:113], v[130:133], v[90:93] cbsz:4 blgp:4
	v_mfma_f32_16x16x128_f8f6f4 v[98:101], v[82:85], v[122:125], v[14:17] cbsz:4 blgp:4
	s_waitcnt lgkmcnt(4)
	v_mfma_f32_16x16x128_f8f6f4 v[98:101], v[102:105], v[134:137], v[98:101] cbsz:4 blgp:4
	v_mfma_f32_16x16x128_f8f6f4 v[106:109], v[94:97], v[122:125], v[10:13] cbsz:4 blgp:4
	s_nop 0
	v_mfma_f32_16x16x128_f8f6f4 v[106:109], v[110:113], v[134:137], v[106:109] cbsz:4 blgp:4
	s_waitcnt lgkmcnt(3)
	v_mfma_f32_16x16x128_f8f6f4 v[118:121], v[82:85], v[176:179], v[14:17] cbsz:4 blgp:4
	s_waitcnt lgkmcnt(1)
	v_mfma_f32_16x16x128_f8f6f4 v[118:121], v[102:105], v[184:187], v[118:121] cbsz:4 blgp:4
	v_mfma_f32_16x16x128_f8f6f4 v[126:129], v[94:97], v[176:179], v[10:13] cbsz:4 blgp:4
	s_nop 0
	v_mfma_f32_16x16x128_f8f6f4 v[126:129], v[110:113], v[184:187], v[126:129] cbsz:4 blgp:4
	v_mfma_f32_16x16x128_f8f6f4 v[138:141], v[82:85], v[180:183], v[14:17] cbsz:4 blgp:4
	s_waitcnt lgkmcnt(0)
	v_mfma_f32_16x16x128_f8f6f4 v[138:141], v[102:105], v[188:191], v[138:141] cbsz:4 blgp:4
	v_mfma_f32_16x16x128_f8f6f4 v[82:85], v[94:97], v[180:183], v[10:13] cbsz:4 blgp:4
	s_nop 0
	v_mfma_f32_16x16x128_f8f6f4 v[82:85], v[110:113], v[188:191], v[82:85] cbsz:4 blgp:4
	v_mfma_f32_16x16x128_f8f6f4 v[94:97], v[142:145], v[114:117], v[6:9] cbsz:4 blgp:4
	s_nop 0
	v_mfma_f32_16x16x128_f8f6f4 v[94:97], v[168:171], v[130:133], v[94:97] cbsz:4 blgp:4
	v_mfma_f32_16x16x128_f8f6f4 v[102:105], v[156:159], v[114:117], v[2:5] cbsz:4 blgp:4
	s_nop 0
	v_mfma_f32_16x16x128_f8f6f4 v[102:105], v[172:175], v[130:133], v[102:105] cbsz:4 blgp:4
	v_mfma_f32_16x16x128_f8f6f4 v[110:113], v[142:145], v[122:125], v[6:9] cbsz:4 blgp:4
	s_nop 0
	v_mfma_f32_16x16x128_f8f6f4 v[110:113], v[168:171], v[134:137], v[110:113] cbsz:4 blgp:4
	v_mfma_f32_16x16x128_f8f6f4 v[114:117], v[156:159], v[122:125], v[2:5] cbsz:4 blgp:4
	s_nop 0
	v_mfma_f32_16x16x128_f8f6f4 v[114:117], v[172:175], v[134:137], v[114:117] cbsz:4 blgp:4
	v_mfma_f32_16x16x128_f8f6f4 v[122:125], v[142:145], v[176:179], v[6:9] cbsz:4 blgp:4
	s_nop 0
	v_mfma_f32_16x16x128_f8f6f4 v[122:125], v[168:171], v[184:187], v[122:125] cbsz:4 blgp:4
	v_mfma_f32_16x16x128_f8f6f4 v[130:133], v[156:159], v[176:179], v[2:5] cbsz:4 blgp:4
	s_nop 0
	v_mfma_f32_16x16x128_f8f6f4 v[130:133], v[172:175], v[184:187], v[130:133] cbsz:4 blgp:4
	v_mfma_f32_16x16x128_f8f6f4 v[134:137], v[142:145], v[180:183], v[6:9] cbsz:4 blgp:4
	s_nop 0
	v_mfma_f32_16x16x128_f8f6f4 v[134:137], v[168:171], v[188:191], v[134:137] cbsz:4 blgp:4
	v_mfma_f32_16x16x128_f8f6f4 v[142:145], v[156:159], v[180:183], v[2:5] cbsz:4 blgp:4
	s_nop 0
	v_mfma_f32_16x16x128_f8f6f4 v[142:145], v[172:175], v[188:191], v[142:145] cbsz:4 blgp:4
	s_setprio 0
	s_barrier
	ds_read_b128 v[156:159], v163 offset:32768
	ds_read_b128 v[168:171], v163 offset:34816
	ds_read_b128 v[172:175], v164 offset:32768
	ds_read_b128 v[176:179], v164 offset:34816
	ds_read_b128 v[180:183], v165 offset:32768
	ds_read_b128 v[184:187], v165 offset:34816
	ds_read_b128 v[188:191], v166 offset:32768
	ds_read_b128 v[192:195], v166 offset:34816
	ds_read_b128 v[196:199], v165 offset:36864
	ds_read_b128 v[200:203], v165 offset:38912
	ds_read_b128 v[204:207], v166 offset:36864
	ds_read_b128 v[208:211], v166 offset:38912
	s_add_u32 s48, s48, s22
	s_addc_u32 s49, s49, s23
	s_mov_b32 m0, s61
	s_nop 0
	global_load_lds_dwordx4 v146, s[48:49]
	s_mov_b32 m0, s62
	s_nop 0
	global_load_lds_dwordx4 v150, s[48:49]
	ds_read_b128 v[212:215], v163 offset:49152
	ds_read_b128 v[216:219], v163 offset:51200
	ds_read_b128 v[220:223], v164 offset:49152
	ds_read_b128 v[224:227], v164 offset:51200
	s_waitcnt vmcnt(8)
	s_waitcnt lgkmcnt(0)
	s_barrier
	s_waitcnt lgkmcnt(0)
	s_setprio 1
	s_waitcnt lgkmcnt(7)
	v_mfma_f32_16x16x128_f8f6f4 v[18:21], v[156:159], v[180:183], v[18:21] cbsz:4 blgp:4
	s_waitcnt lgkmcnt(5)
	v_mfma_f32_16x16x128_f8f6f4 v[18:21], v[172:175], v[188:191], v[18:21] cbsz:4 blgp:4
	v_mfma_f32_16x16x128_f8f6f4 v[22:25], v[168:171], v[180:183], v[22:25] cbsz:4 blgp:4
	s_nop 0
	v_mfma_f32_16x16x128_f8f6f4 v[22:25], v[176:179], v[188:191], v[22:25] cbsz:4 blgp:4
	v_mfma_f32_16x16x128_f8f6f4 v[26:29], v[156:159], v[184:187], v[26:29] cbsz:4 blgp:4
	s_waitcnt lgkmcnt(4)
	v_mfma_f32_16x16x128_f8f6f4 v[26:29], v[172:175], v[192:195], v[26:29] cbsz:4 blgp:4
	v_mfma_f32_16x16x128_f8f6f4 v[30:33], v[168:171], v[184:187], v[30:33] cbsz:4 blgp:4
	s_nop 0
	v_mfma_f32_16x16x128_f8f6f4 v[30:33], v[176:179], v[192:195], v[30:33] cbsz:4 blgp:4
	s_waitcnt lgkmcnt(3)
	v_mfma_f32_16x16x128_f8f6f4 v[34:37], v[156:159], v[196:199], v[34:37] cbsz:4 blgp:4
	s_waitcnt lgkmcnt(1)
	v_mfma_f32_16x16x128_f8f6f4 v[34:37], v[172:175], v[204:207], v[34:37] cbsz:4 blgp:4
	v_mfma_f32_16x16x128_f8f6f4 v[38:41], v[168:171], v[196:199], v[38:41] cbsz:4 blgp:4
	s_nop 0
	v_mfma_f32_16x16x128_f8f6f4 v[38:41], v[176:179], v[204:207], v[38:41] cbsz:4 blgp:4
	v_mfma_f32_16x16x128_f8f6f4 v[42:45], v[156:159], v[200:203], v[42:45] cbsz:4 blgp:4
	s_waitcnt lgkmcnt(0)
	v_mfma_f32_16x16x128_f8f6f4 v[42:45], v[172:175], v[208:211], v[42:45] cbsz:4 blgp:4
	v_mfma_f32_16x16x128_f8f6f4 v[46:49], v[168:171], v[200:203], v[46:49] cbsz:4 blgp:4
	s_nop 0
	v_mfma_f32_16x16x128_f8f6f4 v[46:49], v[176:179], v[208:211], v[46:49] cbsz:4 blgp:4
	s_waitcnt lgkmcnt(3)
	v_mfma_f32_16x16x128_f8f6f4 v[50:53], v[212:215], v[180:183], v[50:53] cbsz:4 blgp:4
	s_waitcnt lgkmcnt(1)
	v_mfma_f32_16x16x128_f8f6f4 v[50:53], v[220:223], v[188:191], v[50:53] cbsz:4 blgp:4
	v_mfma_f32_16x16x128_f8f6f4 v[54:57], v[216:219], v[180:183], v[54:57] cbsz:4 blgp:4
	s_waitcnt lgkmcnt(0)
	v_mfma_f32_16x16x128_f8f6f4 v[54:57], v[224:227], v[188:191], v[54:57] cbsz:4 blgp:4
	v_mfma_f32_16x16x128_f8f6f4 v[58:61], v[212:215], v[184:187], v[58:61] cbsz:4 blgp:4
	s_nop 0
	v_mfma_f32_16x16x128_f8f6f4 v[58:61], v[220:223], v[192:195], v[58:61] cbsz:4 blgp:4
	v_mfma_f32_16x16x128_f8f6f4 v[62:65], v[216:219], v[184:187], v[62:65] cbsz:4 blgp:4
	s_nop 0
	v_mfma_f32_16x16x128_f8f6f4 v[62:65], v[224:227], v[192:195], v[62:65] cbsz:4 blgp:4
	v_mfma_f32_16x16x128_f8f6f4 v[66:69], v[212:215], v[196:199], v[66:69] cbsz:4 blgp:4
	s_nop 0
	v_mfma_f32_16x16x128_f8f6f4 v[66:69], v[220:223], v[204:207], v[66:69] cbsz:4 blgp:4
	v_mfma_f32_16x16x128_f8f6f4 v[70:73], v[216:219], v[196:199], v[70:73] cbsz:4 blgp:4
	s_nop 0
	v_mfma_f32_16x16x128_f8f6f4 v[70:73], v[224:227], v[204:207], v[70:73] cbsz:4 blgp:4
	v_mfma_f32_16x16x128_f8f6f4 v[74:77], v[212:215], v[200:203], v[74:77] cbsz:4 blgp:4
	s_nop 0
	v_mfma_f32_16x16x128_f8f6f4 v[74:77], v[220:223], v[208:211], v[74:77] cbsz:4 blgp:4
	v_mfma_f32_16x16x128_f8f6f4 v[78:81], v[216:219], v[200:203], v[78:81] cbsz:4 blgp:4
	s_nop 0
	v_mfma_f32_16x16x128_f8f6f4 v[78:81], v[224:227], v[208:211], v[78:81] cbsz:4 blgp:4
	s_setprio 0
	s_barrier
	s_mov_b32 m0, s65
	s_nop 0
	global_load_lds_dwordx4 v148, s[44:45]
	s_mov_b32 m0, s66
	s_nop 0
	global_load_lds_dwordx4 v152, s[44:45]
	ds_read_b128 v[180:183], v165 offset:49152
	ds_read_b128 v[184:187], v165 offset:51200
	ds_read_b128 v[188:191], v166 offset:49152
	ds_read_b128 v[192:195], v166 offset:51200
	ds_read_b128 v[196:199], v165 offset:53248
	ds_read_b128 v[200:203], v165 offset:55296
	ds_read_b128 v[204:207], v166 offset:53248
	ds_read_b128 v[208:211], v166 offset:55296
	s_mov_b32 m0, s67
	s_nop 0
	global_load_lds_dwordx4 v146, s[46:47]
	s_mov_b32 m0, s68
	s_nop 0
	global_load_lds_dwordx4 v150, s[46:47]
	s_add_u32 s44, s44, s24
	s_addc_u32 s45, s45, s25
	s_mov_b32 m0, s69
	s_nop 0
	global_load_lds_dwordx4 v148, s[44:45]
	s_mov_b32 m0, s70
	s_nop 0
	global_load_lds_dwordx4 v152, s[44:45]
	s_waitcnt vmcnt(8)
	s_waitcnt lgkmcnt(0)
	s_barrier
	s_setprio 1
	s_waitcnt lgkmcnt(7)
	v_mfma_f32_16x16x128_f8f6f4 v[86:89], v[156:159], v[180:183], v[86:89] cbsz:4 blgp:4
	s_waitcnt lgkmcnt(5)
	v_mfma_f32_16x16x128_f8f6f4 v[86:89], v[172:175], v[188:191], v[86:89] cbsz:4 blgp:4
	v_mfma_f32_16x16x128_f8f6f4 v[90:93], v[168:171], v[180:183], v[90:93] cbsz:4 blgp:4
	s_nop 0
	v_mfma_f32_16x16x128_f8f6f4 v[90:93], v[176:179], v[188:191], v[90:93] cbsz:4 blgp:4
	v_mfma_f32_16x16x128_f8f6f4 v[98:101], v[156:159], v[184:187], v[98:101] cbsz:4 blgp:4
	s_waitcnt lgkmcnt(4)
	v_mfma_f32_16x16x128_f8f6f4 v[98:101], v[172:175], v[192:195], v[98:101] cbsz:4 blgp:4
	v_mfma_f32_16x16x128_f8f6f4 v[106:109], v[168:171], v[184:187], v[106:109] cbsz:4 blgp:4
	s_nop 0
	v_mfma_f32_16x16x128_f8f6f4 v[106:109], v[176:179], v[192:195], v[106:109] cbsz:4 blgp:4
	s_waitcnt lgkmcnt(3)
	v_mfma_f32_16x16x128_f8f6f4 v[118:121], v[156:159], v[196:199], v[118:121] cbsz:4 blgp:4
	s_waitcnt lgkmcnt(1)
	v_mfma_f32_16x16x128_f8f6f4 v[118:121], v[172:175], v[204:207], v[118:121] cbsz:4 blgp:4
	v_mfma_f32_16x16x128_f8f6f4 v[126:129], v[168:171], v[196:199], v[126:129] cbsz:4 blgp:4
	s_nop 0
	v_mfma_f32_16x16x128_f8f6f4 v[126:129], v[176:179], v[204:207], v[126:129] cbsz:4 blgp:4
	v_mfma_f32_16x16x128_f8f6f4 v[138:141], v[156:159], v[200:203], v[138:141] cbsz:4 blgp:4
	s_waitcnt lgkmcnt(0)
	v_mfma_f32_16x16x128_f8f6f4 v[138:141], v[172:175], v[208:211], v[138:141] cbsz:4 blgp:4
	v_mfma_f32_16x16x128_f8f6f4 v[82:85], v[168:171], v[200:203], v[82:85] cbsz:4 blgp:4
	s_nop 0
	v_mfma_f32_16x16x128_f8f6f4 v[82:85], v[176:179], v[208:211], v[82:85] cbsz:4 blgp:4
	v_mfma_f32_16x16x128_f8f6f4 v[94:97], v[212:215], v[180:183], v[94:97] cbsz:4 blgp:4
	s_nop 0
	v_mfma_f32_16x16x128_f8f6f4 v[94:97], v[220:223], v[188:191], v[94:97] cbsz:4 blgp:4
	v_mfma_f32_16x16x128_f8f6f4 v[102:105], v[216:219], v[180:183], v[102:105] cbsz:4 blgp:4
	s_nop 0
	v_mfma_f32_16x16x128_f8f6f4 v[102:105], v[224:227], v[188:191], v[102:105] cbsz:4 blgp:4
	v_mfma_f32_16x16x128_f8f6f4 v[110:113], v[212:215], v[184:187], v[110:113] cbsz:4 blgp:4
	s_nop 0
	v_mfma_f32_16x16x128_f8f6f4 v[110:113], v[220:223], v[192:195], v[110:113] cbsz:4 blgp:4
	v_mfma_f32_16x16x128_f8f6f4 v[114:117], v[216:219], v[184:187], v[114:117] cbsz:4 blgp:4
	s_nop 0
	v_mfma_f32_16x16x128_f8f6f4 v[114:117], v[224:227], v[192:195], v[114:117] cbsz:4 blgp:4
	v_mfma_f32_16x16x128_f8f6f4 v[122:125], v[212:215], v[196:199], v[122:125] cbsz:4 blgp:4
	s_nop 0
	v_mfma_f32_16x16x128_f8f6f4 v[122:125], v[220:223], v[204:207], v[122:125] cbsz:4 blgp:4
	v_mfma_f32_16x16x128_f8f6f4 v[130:133], v[216:219], v[196:199], v[130:133] cbsz:4 blgp:4
	s_nop 0
	v_mfma_f32_16x16x128_f8f6f4 v[130:133], v[224:227], v[204:207], v[130:133] cbsz:4 blgp:4
	v_mfma_f32_16x16x128_f8f6f4 v[134:137], v[212:215], v[200:203], v[134:137] cbsz:4 blgp:4
	s_nop 0
	v_mfma_f32_16x16x128_f8f6f4 v[134:137], v[220:223], v[208:211], v[134:137] cbsz:4 blgp:4
	v_mfma_f32_16x16x128_f8f6f4 v[142:145], v[216:219], v[200:203], v[142:145] cbsz:4 blgp:4
	s_nop 0
	v_mfma_f32_16x16x128_f8f6f4 v[142:145], v[224:227], v[208:211], v[142:145] cbsz:4 blgp:4
	s_setprio 0
	s_andn2_b64 vcc, exec, s[34:35]
	s_barrier
	s_cbranch_vccnz .LBB5_4
	s_ashr_i32 s29, s28, 31
	s_lshl_b64 s[44:45], s[28:29], 10
	s_add_u32 s44, s10, s44
	s_addc_u32 s45, s11, s45
	s_add_u32 s29, s42, 0x200
	s_addc_u32 s79, s43, 0
	s_add_u32 s80, s40, 0x200
	s_addc_u32 s81, s41, 0
	s_add_u32 s40, s82, 0x180
	s_addc_u32 s41, s83, 0
	s_mov_b32 s82, 4
	s_cmp_eq_u32 s64, s82
	s_cselect_b64 s[42:43], -1, 0
	s_cmp_lg_u32 s64, s82
	s_cbranch_scc1 .LBB5_15

.LBB5_15:
	ds_read_b128 v[156:159], v163
	ds_read_b128 v[168:171], v163 offset:2048
	ds_read_b128 v[172:175], v164
	ds_read_b128 v[176:179], v164 offset:2048
	s_and_b64 s[42:43], s[42:43], exec
	s_cselect_b32 s48, s38, s29
	s_cselect_b32 s49, s39, s79
	s_cselect_b32 s51, s5, s81
	s_cselect_b32 s50, s4, s80
	s_add_u32 s46, s48, 0x80
	s_addc_u32 s47, s49, 0
	s_add_u32 s42, s50, 0x80
	s_addc_u32 s43, s51, 0
	ds_read_b128 v[180:183], v165
	ds_read_b128 v[184:187], v165 offset:2048
	ds_read_b128 v[188:191], v166
	ds_read_b128 v[192:195], v166 offset:2048
	ds_read_b128 v[196:199], v165 offset:4096
	ds_read_b128 v[200:203], v165 offset:6144
	ds_read_b128 v[204:207], v166 offset:4096
	ds_read_b128 v[208:211], v166 offset:6144
	s_mov_b32 m0, s71
	s_nop 0
	global_load_lds_dwordx4 v146, s[40:41]
	s_mov_b32 m0, s72
	s_nop 0
	global_load_lds_dwordx4 v150, s[40:41]
	ds_read_b128 v[212:215], v163 offset:16384
	ds_read_b128 v[216:219], v163 offset:18432
	ds_read_b128 v[220:223], v164 offset:16384
	ds_read_b128 v[224:227], v164 offset:18432
	s_waitcnt vmcnt(8)
	s_waitcnt lgkmcnt(0)
	s_barrier
	s_waitcnt lgkmcnt(0)
	s_setprio 1
	s_waitcnt lgkmcnt(7)
	v_mfma_f32_16x16x128_f8f6f4 v[18:21], v[156:159], v[180:183], v[18:21] cbsz:4 blgp:4
	s_waitcnt lgkmcnt(5)
	v_mfma_f32_16x16x128_f8f6f4 v[18:21], v[172:175], v[188:191], v[18:21] cbsz:4 blgp:4
	v_mfma_f32_16x16x128_f8f6f4 v[22:25], v[168:171], v[180:183], v[22:25] cbsz:4 blgp:4
	s_nop 0
	v_mfma_f32_16x16x128_f8f6f4 v[22:25], v[176:179], v[188:191], v[22:25] cbsz:4 blgp:4
	v_mfma_f32_16x16x128_f8f6f4 v[26:29], v[156:159], v[184:187], v[26:29] cbsz:4 blgp:4
	s_waitcnt lgkmcnt(4)
	v_mfma_f32_16x16x128_f8f6f4 v[26:29], v[172:175], v[192:195], v[26:29] cbsz:4 blgp:4
	v_mfma_f32_16x16x128_f8f6f4 v[30:33], v[168:171], v[184:187], v[30:33] cbsz:4 blgp:4
	s_nop 0
	v_mfma_f32_16x16x128_f8f6f4 v[30:33], v[176:179], v[192:195], v[30:33] cbsz:4 blgp:4
	s_waitcnt lgkmcnt(3)
	v_mfma_f32_16x16x128_f8f6f4 v[34:37], v[156:159], v[196:199], v[34:37] cbsz:4 blgp:4
	s_waitcnt lgkmcnt(1)
	v_mfma_f32_16x16x128_f8f6f4 v[34:37], v[172:175], v[204:207], v[34:37] cbsz:4 blgp:4
	v_mfma_f32_16x16x128_f8f6f4 v[38:41], v[168:171], v[196:199], v[38:41] cbsz:4 blgp:4
	s_nop 0
	v_mfma_f32_16x16x128_f8f6f4 v[38:41], v[176:179], v[204:207], v[38:41] cbsz:4 blgp:4
	v_mfma_f32_16x16x128_f8f6f4 v[42:45], v[156:159], v[200:203], v[42:45] cbsz:4 blgp:4
	s_waitcnt lgkmcnt(0)
	v_mfma_f32_16x16x128_f8f6f4 v[42:45], v[172:175], v[208:211], v[42:45] cbsz:4 blgp:4
	v_mfma_f32_16x16x128_f8f6f4 v[46:49], v[168:171], v[200:203], v[46:49] cbsz:4 blgp:4
	s_nop 0
	v_mfma_f32_16x16x128_f8f6f4 v[46:49], v[176:179], v[208:211], v[46:49] cbsz:4 blgp:4
	s_waitcnt lgkmcnt(3)
	v_mfma_f32_16x16x128_f8f6f4 v[50:53], v[212:215], v[180:183], v[50:53] cbsz:4 blgp:4
	s_waitcnt lgkmcnt(1)
	v_mfma_f32_16x16x128_f8f6f4 v[50:53], v[220:223], v[188:191], v[50:53] cbsz:4 blgp:4
	v_mfma_f32_16x16x128_f8f6f4 v[54:57], v[216:219], v[180:183], v[54:57] cbsz:4 blgp:4
	s_waitcnt lgkmcnt(0)
	v_mfma_f32_16x16x128_f8f6f4 v[54:57], v[224:227], v[188:191], v[54:57] cbsz:4 blgp:4
	v_mfma_f32_16x16x128_f8f6f4 v[58:61], v[212:215], v[184:187], v[58:61] cbsz:4 blgp:4
	s_nop 0
	v_mfma_f32_16x16x128_f8f6f4 v[58:61], v[220:223], v[192:195], v[58:61] cbsz:4 blgp:4
	v_mfma_f32_16x16x128_f8f6f4 v[62:65], v[216:219], v[184:187], v[62:65] cbsz:4 blgp:4
	s_nop 0
	v_mfma_f32_16x16x128_f8f6f4 v[62:65], v[224:227], v[192:195], v[62:65] cbsz:4 blgp:4
	v_mfma_f32_16x16x128_f8f6f4 v[66:69], v[212:215], v[196:199], v[66:69] cbsz:4 blgp:4
	s_nop 0
	v_mfma_f32_16x16x128_f8f6f4 v[66:69], v[220:223], v[204:207], v[66:69] cbsz:4 blgp:4
	v_mfma_f32_16x16x128_f8f6f4 v[70:73], v[216:219], v[196:199], v[70:73] cbsz:4 blgp:4
	s_nop 0
	v_mfma_f32_16x16x128_f8f6f4 v[70:73], v[224:227], v[204:207], v[70:73] cbsz:4 blgp:4
	v_mfma_f32_16x16x128_f8f6f4 v[74:77], v[212:215], v[200:203], v[74:77] cbsz:4 blgp:4
	s_nop 0
	v_mfma_f32_16x16x128_f8f6f4 v[74:77], v[220:223], v[208:211], v[74:77] cbsz:4 blgp:4
	v_mfma_f32_16x16x128_f8f6f4 v[78:81], v[216:219], v[200:203], v[78:81] cbsz:4 blgp:4
	s_nop 0
	v_mfma_f32_16x16x128_f8f6f4 v[78:81], v[224:227], v[208:211], v[78:81] cbsz:4 blgp:4
	s_setprio 0
	s_barrier
	s_mov_b32 m0, s56
	s_nop 0
	global_load_lds_dwordx4 v148, s[50:51]
	s_mov_b32 m0, s57
	s_nop 0
	global_load_lds_dwordx4 v152, s[50:51]
	ds_read_b128 v[180:183], v165 offset:16384
	ds_read_b128 v[184:187], v165 offset:18432
	ds_read_b128 v[188:191], v166 offset:16384
	ds_read_b128 v[192:195], v166 offset:18432
	ds_read_b128 v[196:199], v165 offset:20480
	ds_read_b128 v[200:203], v165 offset:22528
	ds_read_b128 v[204:207], v166 offset:20480
	ds_read_b128 v[208:211], v166 offset:22528
	s_mov_b32 m0, s55
	s_nop 0
	global_load_lds_dwordx4 v146, s[48:49]
	s_mov_b32 m0, s58
	s_nop 0
	global_load_lds_dwordx4 v150, s[48:49]
	s_add_u32 s50, s50, s24
	s_addc_u32 s51, s51, s25
	s_mov_b32 m0, s59
	s_nop 0
	global_load_lds_dwordx4 v148, s[50:51]
	s_mov_b32 m0, s60
	s_nop 0
	global_load_lds_dwordx4 v152, s[50:51]
	s_waitcnt vmcnt(8)
	s_waitcnt lgkmcnt(0)
	s_barrier
	s_setprio 1
	s_waitcnt lgkmcnt(7)
	v_mfma_f32_16x16x128_f8f6f4 v[86:89], v[156:159], v[180:183], v[86:89] cbsz:4 blgp:4
	s_waitcnt lgkmcnt(5)
	v_mfma_f32_16x16x128_f8f6f4 v[86:89], v[172:175], v[188:191], v[86:89] cbsz:4 blgp:4
	v_mfma_f32_16x16x128_f8f6f4 v[90:93], v[168:171], v[180:183], v[90:93] cbsz:4 blgp:4
	s_nop 0
	v_mfma_f32_16x16x128_f8f6f4 v[90:93], v[176:179], v[188:191], v[90:93] cbsz:4 blgp:4
	v_mfma_f32_16x16x128_f8f6f4 v[98:101], v[156:159], v[184:187], v[98:101] cbsz:4 blgp:4
	s_waitcnt lgkmcnt(4)
	v_mfma_f32_16x16x128_f8f6f4 v[98:101], v[172:175], v[192:195], v[98:101] cbsz:4 blgp:4
	v_mfma_f32_16x16x128_f8f6f4 v[106:109], v[168:171], v[184:187], v[106:109] cbsz:4 blgp:4
	s_nop 0
	v_mfma_f32_16x16x128_f8f6f4 v[106:109], v[176:179], v[192:195], v[106:109] cbsz:4 blgp:4
	s_waitcnt lgkmcnt(3)
	v_mfma_f32_16x16x128_f8f6f4 v[118:121], v[156:159], v[196:199], v[118:121] cbsz:4 blgp:4
	s_waitcnt lgkmcnt(1)
	v_mfma_f32_16x16x128_f8f6f4 v[118:121], v[172:175], v[204:207], v[118:121] cbsz:4 blgp:4
	v_mfma_f32_16x16x128_f8f6f4 v[126:129], v[168:171], v[196:199], v[126:129] cbsz:4 blgp:4
	s_nop 0
	v_mfma_f32_16x16x128_f8f6f4 v[126:129], v[176:179], v[204:207], v[126:129] cbsz:4 blgp:4
	v_mfma_f32_16x16x128_f8f6f4 v[138:141], v[156:159], v[200:203], v[138:141] cbsz:4 blgp:4
	s_waitcnt lgkmcnt(0)
	v_mfma_f32_16x16x128_f8f6f4 v[138:141], v[172:175], v[208:211], v[138:141] cbsz:4 blgp:4
	v_mfma_f32_16x16x128_f8f6f4 v[82:85], v[168:171], v[200:203], v[82:85] cbsz:4 blgp:4
	s_nop 0
	v_mfma_f32_16x16x128_f8f6f4 v[82:85], v[176:179], v[208:211], v[82:85] cbsz:4 blgp:4
	v_mfma_f32_16x16x128_f8f6f4 v[94:97], v[212:215], v[180:183], v[94:97] cbsz:4 blgp:4
	s_nop 0
	v_mfma_f32_16x16x128_f8f6f4 v[94:97], v[220:223], v[188:191], v[94:97] cbsz:4 blgp:4
	v_mfma_f32_16x16x128_f8f6f4 v[102:105], v[216:219], v[180:183], v[102:105] cbsz:4 blgp:4
	s_nop 0
	v_mfma_f32_16x16x128_f8f6f4 v[102:105], v[224:227], v[188:191], v[102:105] cbsz:4 blgp:4
	v_mfma_f32_16x16x128_f8f6f4 v[110:113], v[212:215], v[184:187], v[110:113] cbsz:4 blgp:4
	s_nop 0
	v_mfma_f32_16x16x128_f8f6f4 v[110:113], v[220:223], v[192:195], v[110:113] cbsz:4 blgp:4
	v_mfma_f32_16x16x128_f8f6f4 v[114:117], v[216:219], v[184:187], v[114:117] cbsz:4 blgp:4
	s_nop 0
	v_mfma_f32_16x16x128_f8f6f4 v[114:117], v[224:227], v[192:195], v[114:117] cbsz:4 blgp:4
	v_mfma_f32_16x16x128_f8f6f4 v[122:125], v[212:215], v[196:199], v[122:125] cbsz:4 blgp:4
	s_nop 0
	v_mfma_f32_16x16x128_f8f6f4 v[122:125], v[220:223], v[204:207], v[122:125] cbsz:4 blgp:4
	v_mfma_f32_16x16x128_f8f6f4 v[130:133], v[216:219], v[196:199], v[130:133] cbsz:4 blgp:4
	s_nop 0
	v_mfma_f32_16x16x128_f8f6f4 v[130:133], v[224:227], v[204:207], v[130:133] cbsz:4 blgp:4
	v_mfma_f32_16x16x128_f8f6f4 v[134:137], v[212:215], v[200:203], v[134:137] cbsz:4 blgp:4
	s_nop 0
	v_mfma_f32_16x16x128_f8f6f4 v[134:137], v[220:223], v[208:211], v[134:137] cbsz:4 blgp:4
	v_mfma_f32_16x16x128_f8f6f4 v[142:145], v[216:219], v[200:203], v[142:145] cbsz:4 blgp:4
	s_nop 0
	v_mfma_f32_16x16x128_f8f6f4 v[142:145], v[224:227], v[208:211], v[142:145] cbsz:4 blgp:4
	s_setprio 0
	s_barrier
	ds_read_b128 v[156:159], v163 offset:32768
	ds_read_b128 v[168:171], v163 offset:34816
	ds_read_b128 v[172:175], v164 offset:32768
	ds_read_b128 v[176:179], v164 offset:34816
	ds_read_b128 v[180:183], v165 offset:32768
	ds_read_b128 v[184:187], v165 offset:34816
	ds_read_b128 v[188:191], v166 offset:32768
	ds_read_b128 v[192:195], v166 offset:34816
	ds_read_b128 v[196:199], v165 offset:36864
	ds_read_b128 v[200:203], v165 offset:38912
	ds_read_b128 v[204:207], v166 offset:36864
	ds_read_b128 v[208:211], v166 offset:38912
	s_add_u32 s48, s48, s22
	s_addc_u32 s49, s49, s23
	s_mov_b32 m0, s61
	s_nop 0
	global_load_lds_dwordx4 v146, s[48:49]
	s_mov_b32 m0, s62
	s_nop 0
	global_load_lds_dwordx4 v150, s[48:49]
	ds_read_b128 v[212:215], v163 offset:49152
	ds_read_b128 v[216:219], v163 offset:51200
	ds_read_b128 v[220:223], v164 offset:49152
	ds_read_b128 v[224:227], v164 offset:51200
	s_waitcnt vmcnt(8)
	s_waitcnt lgkmcnt(0)
	s_barrier
	s_waitcnt lgkmcnt(0)
	s_setprio 1
	s_waitcnt lgkmcnt(7)
	v_mfma_f32_16x16x128_f8f6f4 v[18:21], v[156:159], v[180:183], v[18:21] cbsz:4 blgp:4
	s_waitcnt lgkmcnt(5)
	v_mfma_f32_16x16x128_f8f6f4 v[18:21], v[172:175], v[188:191], v[18:21] cbsz:4 blgp:4
	v_mfma_f32_16x16x128_f8f6f4 v[22:25], v[168:171], v[180:183], v[22:25] cbsz:4 blgp:4
	s_nop 0
	v_mfma_f32_16x16x128_f8f6f4 v[22:25], v[176:179], v[188:191], v[22:25] cbsz:4 blgp:4
	v_mfma_f32_16x16x128_f8f6f4 v[26:29], v[156:159], v[184:187], v[26:29] cbsz:4 blgp:4
	s_waitcnt lgkmcnt(4)
	v_mfma_f32_16x16x128_f8f6f4 v[26:29], v[172:175], v[192:195], v[26:29] cbsz:4 blgp:4
	v_mfma_f32_16x16x128_f8f6f4 v[30:33], v[168:171], v[184:187], v[30:33] cbsz:4 blgp:4
	s_nop 0
	v_mfma_f32_16x16x128_f8f6f4 v[30:33], v[176:179], v[192:195], v[30:33] cbsz:4 blgp:4
	s_waitcnt lgkmcnt(3)
	v_mfma_f32_16x16x128_f8f6f4 v[34:37], v[156:159], v[196:199], v[34:37] cbsz:4 blgp:4
	s_waitcnt lgkmcnt(1)
	v_mfma_f32_16x16x128_f8f6f4 v[34:37], v[172:175], v[204:207], v[34:37] cbsz:4 blgp:4
	v_mfma_f32_16x16x128_f8f6f4 v[38:41], v[168:171], v[196:199], v[38:41] cbsz:4 blgp:4
	s_nop 0
	v_mfma_f32_16x16x128_f8f6f4 v[38:41], v[176:179], v[204:207], v[38:41] cbsz:4 blgp:4
	v_mfma_f32_16x16x128_f8f6f4 v[42:45], v[156:159], v[200:203], v[42:45] cbsz:4 blgp:4
	s_waitcnt lgkmcnt(0)
	v_mfma_f32_16x16x128_f8f6f4 v[42:45], v[172:175], v[208:211], v[42:45] cbsz:4 blgp:4
	v_mfma_f32_16x16x128_f8f6f4 v[46:49], v[168:171], v[200:203], v[46:49] cbsz:4 blgp:4
	s_nop 0
	v_mfma_f32_16x16x128_f8f6f4 v[46:49], v[176:179], v[208:211], v[46:49] cbsz:4 blgp:4
	s_waitcnt lgkmcnt(3)
	v_mfma_f32_16x16x128_f8f6f4 v[50:53], v[212:215], v[180:183], v[50:53] cbsz:4 blgp:4
	s_waitcnt lgkmcnt(1)
	v_mfma_f32_16x16x128_f8f6f4 v[50:53], v[220:223], v[188:191], v[50:53] cbsz:4 blgp:4
	v_mfma_f32_16x16x128_f8f6f4 v[54:57], v[216:219], v[180:183], v[54:57] cbsz:4 blgp:4
	s_waitcnt lgkmcnt(0)
	v_mfma_f32_16x16x128_f8f6f4 v[54:57], v[224:227], v[188:191], v[54:57] cbsz:4 blgp:4
	v_mfma_f32_16x16x128_f8f6f4 v[58:61], v[212:215], v[184:187], v[58:61] cbsz:4 blgp:4
	s_nop 0
	v_mfma_f32_16x16x128_f8f6f4 v[58:61], v[220:223], v[192:195], v[58:61] cbsz:4 blgp:4
	v_mfma_f32_16x16x128_f8f6f4 v[62:65], v[216:219], v[184:187], v[62:65] cbsz:4 blgp:4
	s_nop 0
	v_mfma_f32_16x16x128_f8f6f4 v[62:65], v[224:227], v[192:195], v[62:65] cbsz:4 blgp:4
	v_mfma_f32_16x16x128_f8f6f4 v[66:69], v[212:215], v[196:199], v[66:69] cbsz:4 blgp:4
	s_nop 0
	v_mfma_f32_16x16x128_f8f6f4 v[66:69], v[220:223], v[204:207], v[66:69] cbsz:4 blgp:4
	v_mfma_f32_16x16x128_f8f6f4 v[70:73], v[216:219], v[196:199], v[70:73] cbsz:4 blgp:4
	s_nop 0
	v_mfma_f32_16x16x128_f8f6f4 v[70:73], v[224:227], v[204:207], v[70:73] cbsz:4 blgp:4
	v_mfma_f32_16x16x128_f8f6f4 v[74:77], v[212:215], v[200:203], v[74:77] cbsz:4 blgp:4
	s_nop 0
	v_mfma_f32_16x16x128_f8f6f4 v[74:77], v[220:223], v[208:211], v[74:77] cbsz:4 blgp:4
	v_mfma_f32_16x16x128_f8f6f4 v[78:81], v[216:219], v[200:203], v[78:81] cbsz:4 blgp:4
	s_nop 0
	v_mfma_f32_16x16x128_f8f6f4 v[78:81], v[224:227], v[208:211], v[78:81] cbsz:4 blgp:4
	s_setprio 0
	s_barrier
	s_mov_b32 m0, s65
	s_nop 0
	global_load_lds_dwordx4 v148, s[42:43]
	s_mov_b32 m0, s66
	s_nop 0
	global_load_lds_dwordx4 v152, s[42:43]
	ds_read_b128 v[180:183], v165 offset:49152
	ds_read_b128 v[184:187], v165 offset:51200
	ds_read_b128 v[188:191], v166 offset:49152
	ds_read_b128 v[192:195], v166 offset:51200
	ds_read_b128 v[196:199], v165 offset:53248
	ds_read_b128 v[200:203], v165 offset:55296
	ds_read_b128 v[204:207], v166 offset:53248
	ds_read_b128 v[208:211], v166 offset:55296
	s_mov_b32 m0, s67
	s_nop 0
	global_load_lds_dwordx4 v146, s[46:47]
	s_mov_b32 m0, s68
	s_nop 0
	global_load_lds_dwordx4 v150, s[46:47]
	s_add_u32 s42, s42, s24
	s_addc_u32 s43, s43, s25
	s_mov_b32 m0, s69
	s_nop 0
	global_load_lds_dwordx4 v148, s[42:43]
	s_mov_b32 m0, s70
	s_nop 0
	global_load_lds_dwordx4 v152, s[42:43]
	s_waitcnt vmcnt(8)
	s_waitcnt lgkmcnt(0)
	s_barrier
	s_setprio 1
	s_waitcnt lgkmcnt(7)
	v_mfma_f32_16x16x128_f8f6f4 v[86:89], v[156:159], v[180:183], v[86:89] cbsz:4 blgp:4
	s_waitcnt lgkmcnt(5)
	v_mfma_f32_16x16x128_f8f6f4 v[86:89], v[172:175], v[188:191], v[86:89] cbsz:4 blgp:4
	v_mfma_f32_16x16x128_f8f6f4 v[90:93], v[168:171], v[180:183], v[90:93] cbsz:4 blgp:4
	s_nop 0
	v_mfma_f32_16x16x128_f8f6f4 v[90:93], v[176:179], v[188:191], v[90:93] cbsz:4 blgp:4
	v_mfma_f32_16x16x128_f8f6f4 v[98:101], v[156:159], v[184:187], v[98:101] cbsz:4 blgp:4
	s_waitcnt lgkmcnt(4)
	v_mfma_f32_16x16x128_f8f6f4 v[98:101], v[172:175], v[192:195], v[98:101] cbsz:4 blgp:4
	v_mfma_f32_16x16x128_f8f6f4 v[106:109], v[168:171], v[184:187], v[106:109] cbsz:4 blgp:4
	s_nop 0
	v_mfma_f32_16x16x128_f8f6f4 v[106:109], v[176:179], v[192:195], v[106:109] cbsz:4 blgp:4
	s_waitcnt lgkmcnt(3)
	v_mfma_f32_16x16x128_f8f6f4 v[118:121], v[156:159], v[196:199], v[118:121] cbsz:4 blgp:4
	s_waitcnt lgkmcnt(1)
	v_mfma_f32_16x16x128_f8f6f4 v[118:121], v[172:175], v[204:207], v[118:121] cbsz:4 blgp:4
	v_mfma_f32_16x16x128_f8f6f4 v[126:129], v[168:171], v[196:199], v[126:129] cbsz:4 blgp:4
	s_nop 0
	v_mfma_f32_16x16x128_f8f6f4 v[126:129], v[176:179], v[204:207], v[126:129] cbsz:4 blgp:4
	v_mfma_f32_16x16x128_f8f6f4 v[138:141], v[156:159], v[200:203], v[138:141] cbsz:4 blgp:4
	s_waitcnt lgkmcnt(0)
	v_mfma_f32_16x16x128_f8f6f4 v[138:141], v[172:175], v[208:211], v[138:141] cbsz:4 blgp:4
	v_mfma_f32_16x16x128_f8f6f4 v[82:85], v[168:171], v[200:203], v[82:85] cbsz:4 blgp:4
	s_nop 0
	v_mfma_f32_16x16x128_f8f6f4 v[82:85], v[176:179], v[208:211], v[82:85] cbsz:4 blgp:4
	v_mfma_f32_16x16x128_f8f6f4 v[94:97], v[212:215], v[180:183], v[94:97] cbsz:4 blgp:4
	s_nop 0
	v_mfma_f32_16x16x128_f8f6f4 v[94:97], v[220:223], v[188:191], v[94:97] cbsz:4 blgp:4
	v_mfma_f32_16x16x128_f8f6f4 v[102:105], v[216:219], v[180:183], v[102:105] cbsz:4 blgp:4
	s_nop 0
	v_mfma_f32_16x16x128_f8f6f4 v[102:105], v[224:227], v[188:191], v[102:105] cbsz:4 blgp:4
	v_mfma_f32_16x16x128_f8f6f4 v[110:113], v[212:215], v[184:187], v[110:113] cbsz:4 blgp:4
	s_nop 0
	v_mfma_f32_16x16x128_f8f6f4 v[110:113], v[220:223], v[192:195], v[110:113] cbsz:4 blgp:4
	v_mfma_f32_16x16x128_f8f6f4 v[114:117], v[216:219], v[184:187], v[114:117] cbsz:4 blgp:4
	s_nop 0
	v_mfma_f32_16x16x128_f8f6f4 v[114:117], v[224:227], v[192:195], v[114:117] cbsz:4 blgp:4
	v_mfma_f32_16x16x128_f8f6f4 v[122:125], v[212:215], v[196:199], v[122:125] cbsz:4 blgp:4
	s_nop 0
	v_mfma_f32_16x16x128_f8f6f4 v[122:125], v[220:223], v[204:207], v[122:125] cbsz:4 blgp:4
	v_mfma_f32_16x16x128_f8f6f4 v[130:133], v[216:219], v[196:199], v[130:133] cbsz:4 blgp:4
	s_nop 0
	v_mfma_f32_16x16x128_f8f6f4 v[130:133], v[224:227], v[204:207], v[130:133] cbsz:4 blgp:4
	v_mfma_f32_16x16x128_f8f6f4 v[134:137], v[212:215], v[200:203], v[134:137] cbsz:4 blgp:4
	s_nop 0
	v_mfma_f32_16x16x128_f8f6f4 v[134:137], v[220:223], v[208:211], v[134:137] cbsz:4 blgp:4
	v_mfma_f32_16x16x128_f8f6f4 v[142:145], v[216:219], v[200:203], v[142:145] cbsz:4 blgp:4
	s_nop 0
	v_mfma_f32_16x16x128_f8f6f4 v[142:145], v[224:227], v[208:211], v[142:145] cbsz:4 blgp:4
	s_setprio 0
	s_add_i32 s42, s82, 2
	s_add_u32 s29, s29, 0x100
	s_addc_u32 s79, s79, 0
	s_add_u32 s80, s80, 0x100
	s_addc_u32 s81, s81, 0
	s_add_u32 s40, s40, 0x100
	s_addc_u32 s41, s41, 0
	s_cmp_ge_i32 s82, s64
	s_barrier
	s_cbranch_scc1 .LBB5_4
	s_mov_b32 s82, s42
	s_cmp_eq_u32 s64, s82
	s_cselect_b64 s[42:43], -1, 0
	s_cmp_lg_u32 s64, s82
	s_cbranch_scc0 .LBB5_14
	s_branch .LBB5_15

.LBB6_15:
	s_add_u32 s82, s36, s20
	s_addc_u32 s83, s37, s21
	s_add_u32 s31, s36, 0x100
	s_addc_u32 s39, s37, 0
	s_and_b64 s[40:41], s[12:13], exec
	ds_read_b128 v[82:85], v169
	ds_read_b128 v[94:97], v169 offset:2048
	ds_read_b128 v[102:105], v178
	ds_read_b128 v[110:113], v178 offset:2048
	s_cselect_b32 s45, s5, s39
	s_cselect_b32 s44, s4, s31
	s_add_u32 s31, s34, 0x100
	s_addc_u32 s39, s35, 0
	s_and_b64 s[40:41], s[12:13], exec
	s_cselect_b32 s47, s7, s39
	s_cselect_b32 s46, s6, s31
	s_add_u32 s42, s44, 0x80
	s_addc_u32 s43, s45, 0
	s_add_u32 s40, s46, 0x80
	s_addc_u32 s41, s47, 0
	ds_read_b128 v[58:61], v179
	ds_read_b128 v[66:69], v179 offset:2048
	ds_read_b128 v[62:65], v180
	ds_read_b128 v[70:73], v180 offset:2048
	ds_read_b128 v[74:77], v179 offset:4096
	ds_read_b128 v[86:89], v179 offset:6144
	ds_read_b128 v[78:81], v180 offset:4096
	ds_read_b128 v[90:93], v180 offset:6144
	s_add_u32 s84, s82, 0x80
	s_addc_u32 s85, s83, 0
	s_mov_b32 m0, s68
	s_nop 0
	global_load_lds_dwordx4 v162, s[84:85]
	s_mov_b32 m0, s69
	s_nop 0
	global_load_lds_dwordx4 v166, s[84:85]
	ds_read_b128 v[142:145], v169 offset:16384
	ds_read_b128 v[146:149], v169 offset:18432
	ds_read_b128 v[150:153], v178 offset:16384
	ds_read_b128 v[154:157], v178 offset:18432
	s_waitcnt vmcnt(8)
	s_waitcnt lgkmcnt(0)
	s_barrier
	s_waitcnt lgkmcnt(0)
	s_waitcnt vmcnt(16)
	v_mov_b32_e32 v171, v170
	v_pk_mul_f32 v[16:17], v[170:171], v[16:17]
	v_pk_mul_f32 v[14:15], v[172:173], v[14:15]
	v_pk_mul_f32 v[12:13], v[170:171], v[12:13]
	v_pk_mul_f32 v[10:11], v[172:173], v[10:11]
	v_pk_mul_f32 v[8:9], v[170:171], v[8:9]
	v_pk_mul_f32 v[6:7], v[172:173], v[6:7]
	v_pk_mul_f32 v[4:5], v[170:171], v[4:5]
	v_pk_mul_f32 v[2:3], v[172:173], v[2:3]
	s_setprio 1
	s_waitcnt lgkmcnt(7)
	v_mfma_f32_16x16x128_f8f6f4 v[18:21], v[82:85], v[58:61], v[14:17] cbsz:4 blgp:4
	s_waitcnt lgkmcnt(5)
	v_mfma_f32_16x16x128_f8f6f4 v[18:21], v[102:105], v[62:65], v[18:21] cbsz:4 blgp:4
	v_mfma_f32_16x16x128_f8f6f4 v[22:25], v[94:97], v[58:61], v[10:13] cbsz:4 blgp:4
	s_nop 0
	v_mfma_f32_16x16x128_f8f6f4 v[22:25], v[110:113], v[62:65], v[22:25] cbsz:4 blgp:4
	v_mfma_f32_16x16x128_f8f6f4 v[26:29], v[82:85], v[66:69], v[14:17] cbsz:4 blgp:4
	s_waitcnt lgkmcnt(4)
	v_mfma_f32_16x16x128_f8f6f4 v[26:29], v[102:105], v[70:73], v[26:29] cbsz:4 blgp:4
	v_mfma_f32_16x16x128_f8f6f4 v[30:33], v[94:97], v[66:69], v[10:13] cbsz:4 blgp:4
	s_nop 0
	v_mfma_f32_16x16x128_f8f6f4 v[30:33], v[110:113], v[70:73], v[30:33] cbsz:4 blgp:4
	s_waitcnt lgkmcnt(3)
	v_mfma_f32_16x16x128_f8f6f4 v[34:37], v[82:85], v[74:77], v[14:17] cbsz:4 blgp:4
	s_waitcnt lgkmcnt(1)
	v_mfma_f32_16x16x128_f8f6f4 v[34:37], v[102:105], v[78:81], v[34:37] cbsz:4 blgp:4
	v_mfma_f32_16x16x128_f8f6f4 v[38:41], v[94:97], v[74:77], v[10:13] cbsz:4 blgp:4
	s_nop 0
	v_mfma_f32_16x16x128_f8f6f4 v[38:41], v[110:113], v[78:81], v[38:41] cbsz:4 blgp:4
	v_mfma_f32_16x16x128_f8f6f4 v[42:45], v[82:85], v[86:89], v[14:17] cbsz:4 blgp:4
	s_waitcnt lgkmcnt(0)
	v_mfma_f32_16x16x128_f8f6f4 v[42:45], v[102:105], v[90:93], v[42:45] cbsz:4 blgp:4
	v_mfma_f32_16x16x128_f8f6f4 v[46:49], v[94:97], v[86:89], v[10:13] cbsz:4 blgp:4
	s_nop 0
	v_mfma_f32_16x16x128_f8f6f4 v[46:49], v[110:113], v[90:93], v[46:49] cbsz:4 blgp:4
	s_waitcnt lgkmcnt(3)
	v_mfma_f32_16x16x128_f8f6f4 v[50:53], v[142:145], v[58:61], v[6:9] cbsz:4 blgp:4
	s_waitcnt lgkmcnt(1)
	v_mfma_f32_16x16x128_f8f6f4 v[50:53], v[150:153], v[62:65], v[50:53] cbsz:4 blgp:4
	v_mfma_f32_16x16x128_f8f6f4 v[54:57], v[146:149], v[58:61], v[2:5] cbsz:4 blgp:4
	s_waitcnt lgkmcnt(0)
	v_mfma_f32_16x16x128_f8f6f4 v[54:57], v[154:157], v[62:65], v[54:57] cbsz:4 blgp:4
	v_mfma_f32_16x16x128_f8f6f4 v[58:61], v[142:145], v[66:69], v[6:9] cbsz:4 blgp:4
	s_nop 0
	v_mfma_f32_16x16x128_f8f6f4 v[58:61], v[150:153], v[70:73], v[58:61] cbsz:4 blgp:4
	v_mfma_f32_16x16x128_f8f6f4 v[62:65], v[146:149], v[66:69], v[2:5] cbsz:4 blgp:4
	s_nop 0
	v_mfma_f32_16x16x128_f8f6f4 v[62:65], v[154:157], v[70:73], v[62:65] cbsz:4 blgp:4
	v_mfma_f32_16x16x128_f8f6f4 v[66:69], v[142:145], v[74:77], v[6:9] cbsz:4 blgp:4
	s_nop 0
	v_mfma_f32_16x16x128_f8f6f4 v[66:69], v[150:153], v[78:81], v[66:69] cbsz:4 blgp:4
	v_mfma_f32_16x16x128_f8f6f4 v[70:73], v[146:149], v[74:77], v[2:5] cbsz:4 blgp:4
	s_nop 0
	v_mfma_f32_16x16x128_f8f6f4 v[70:73], v[154:157], v[78:81], v[70:73] cbsz:4 blgp:4
	v_mfma_f32_16x16x128_f8f6f4 v[74:77], v[142:145], v[86:89], v[6:9] cbsz:4 blgp:4
	s_nop 0
	v_mfma_f32_16x16x128_f8f6f4 v[74:77], v[150:153], v[90:93], v[74:77] cbsz:4 blgp:4
	v_mfma_f32_16x16x128_f8f6f4 v[78:81], v[146:149], v[86:89], v[2:5] cbsz:4 blgp:4
	s_nop 0
	v_mfma_f32_16x16x128_f8f6f4 v[78:81], v[154:157], v[90:93], v[78:81] cbsz:4 blgp:4
	s_setprio 0
	s_barrier
	s_mov_b32 m0, s54
	s_nop 0
	global_load_lds_dwordx4 v164, s[46:47]
	s_mov_b32 m0, s55
	s_nop 0
	global_load_lds_dwordx4 v168, s[46:47]
	ds_read_b128 v[114:117], v179 offset:16384
	ds_read_b128 v[122:125], v179 offset:18432
	ds_read_b128 v[130:133], v180 offset:16384
	ds_read_b128 v[134:137], v180 offset:18432
	ds_read_b128 v[158:161], v179 offset:20480
	ds_read_b128 v[182:185], v179 offset:22528
	ds_read_b128 v[186:189], v180 offset:20480
	ds_read_b128 v[190:193], v180 offset:22528
	s_mov_b32 m0, s53
	s_nop 0
	global_load_lds_dwordx4 v162, s[44:45]
	s_mov_b32 m0, s56
	s_nop 0
	global_load_lds_dwordx4 v166, s[44:45]
	s_add_u32 s46, s46, s22
	s_addc_u32 s47, s47, s23
	s_mov_b32 m0, s57
	s_nop 0
	global_load_lds_dwordx4 v164, s[46:47]
	s_mov_b32 m0, s58
	s_nop 0
	global_load_lds_dwordx4 v168, s[46:47]
	s_waitcnt vmcnt(8)
	s_waitcnt lgkmcnt(0)
	s_barrier
	s_setprio 1
	s_waitcnt lgkmcnt(7)
	v_mfma_f32_16x16x128_f8f6f4 v[86:89], v[82:85], v[114:117], v[14:17] cbsz:4 blgp:4
	s_waitcnt lgkmcnt(5)
	v_mfma_f32_16x16x128_f8f6f4 v[86:89], v[102:105], v[130:133], v[86:89] cbsz:4 blgp:4
	v_mfma_f32_16x16x128_f8f6f4 v[90:93], v[94:97], v[114:117], v[10:13] cbsz:4 blgp:4
	s_nop 0
	v_mfma_f32_16x16x128_f8f6f4 v[90:93], v[110:113], v[130:133], v[90:93] cbsz:4 blgp:4
	v_mfma_f32_16x16x128_f8f6f4 v[98:101], v[82:85], v[122:125], v[14:17] cbsz:4 blgp:4
	s_waitcnt lgkmcnt(4)
	v_mfma_f32_16x16x128_f8f6f4 v[98:101], v[102:105], v[134:137], v[98:101] cbsz:4 blgp:4
	v_mfma_f32_16x16x128_f8f6f4 v[106:109], v[94:97], v[122:125], v[10:13] cbsz:4 blgp:4
	s_nop 0
	v_mfma_f32_16x16x128_f8f6f4 v[106:109], v[110:113], v[134:137], v[106:109] cbsz:4 blgp:4
	s_waitcnt lgkmcnt(3)
	v_mfma_f32_16x16x128_f8f6f4 v[118:121], v[82:85], v[158:161], v[14:17] cbsz:4 blgp:4
	s_waitcnt lgkmcnt(1)
	v_mfma_f32_16x16x128_f8f6f4 v[118:121], v[102:105], v[186:189], v[118:121] cbsz:4 blgp:4
	v_mfma_f32_16x16x128_f8f6f4 v[126:129], v[94:97], v[158:161], v[10:13] cbsz:4 blgp:4
	s_nop 0
	v_mfma_f32_16x16x128_f8f6f4 v[126:129], v[110:113], v[186:189], v[126:129] cbsz:4 blgp:4
	v_mfma_f32_16x16x128_f8f6f4 v[138:141], v[82:85], v[182:185], v[14:17] cbsz:4 blgp:4
	s_waitcnt lgkmcnt(0)
	v_mfma_f32_16x16x128_f8f6f4 v[138:141], v[102:105], v[190:193], v[138:141] cbsz:4 blgp:4
	v_mfma_f32_16x16x128_f8f6f4 v[82:85], v[94:97], v[182:185], v[10:13] cbsz:4 blgp:4
	s_nop 0
	v_mfma_f32_16x16x128_f8f6f4 v[82:85], v[110:113], v[190:193], v[82:85] cbsz:4 blgp:4
	v_mfma_f32_16x16x128_f8f6f4 v[94:97], v[142:145], v[114:117], v[6:9] cbsz:4 blgp:4
	s_nop 0
	v_mfma_f32_16x16x128_f8f6f4 v[94:97], v[150:153], v[130:133], v[94:97] cbsz:4 blgp:4
	v_mfma_f32_16x16x128_f8f6f4 v[102:105], v[146:149], v[114:117], v[2:5] cbsz:4 blgp:4
	s_nop 0
	v_mfma_f32_16x16x128_f8f6f4 v[102:105], v[154:157], v[130:133], v[102:105] cbsz:4 blgp:4
	v_mfma_f32_16x16x128_f8f6f4 v[110:113], v[142:145], v[122:125], v[6:9] cbsz:4 blgp:4
	s_nop 0
	v_mfma_f32_16x16x128_f8f6f4 v[110:113], v[150:153], v[134:137], v[110:113] cbsz:4 blgp:4
	v_mfma_f32_16x16x128_f8f6f4 v[114:117], v[146:149], v[122:125], v[2:5] cbsz:4 blgp:4
	s_nop 0
	v_mfma_f32_16x16x128_f8f6f4 v[114:117], v[154:157], v[134:137], v[114:117] cbsz:4 blgp:4
	v_mfma_f32_16x16x128_f8f6f4 v[122:125], v[142:145], v[158:161], v[6:9] cbsz:4 blgp:4
	s_nop 0
	v_mfma_f32_16x16x128_f8f6f4 v[122:125], v[150:153], v[186:189], v[122:125] cbsz:4 blgp:4
	v_mfma_f32_16x16x128_f8f6f4 v[130:133], v[146:149], v[158:161], v[2:5] cbsz:4 blgp:4
	s_nop 0
	v_mfma_f32_16x16x128_f8f6f4 v[130:133], v[154:157], v[186:189], v[130:133] cbsz:4 blgp:4
	v_mfma_f32_16x16x128_f8f6f4 v[134:137], v[142:145], v[182:185], v[6:9] cbsz:4 blgp:4
	s_nop 0
	v_mfma_f32_16x16x128_f8f6f4 v[134:137], v[150:153], v[190:193], v[134:137] cbsz:4 blgp:4
	v_mfma_f32_16x16x128_f8f6f4 v[142:145], v[146:149], v[182:185], v[2:5] cbsz:4 blgp:4
	s_nop 0
	v_mfma_f32_16x16x128_f8f6f4 v[142:145], v[154:157], v[190:193], v[142:145] cbsz:4 blgp:4
	s_setprio 0
	s_barrier
	ds_read_b128 v[146:149], v169 offset:32768
	ds_read_b128 v[150:153], v169 offset:34816
	ds_read_b128 v[154:157], v178 offset:32768
	ds_read_b128 v[158:161], v178 offset:34816
	ds_read_b128 v[182:185], v179 offset:32768
	ds_read_b128 v[186:189], v179 offset:34816
	ds_read_b128 v[190:193], v180 offset:32768
	ds_read_b128 v[194:197], v180 offset:34816
	ds_read_b128 v[198:201], v179 offset:36864
	ds_read_b128 v[202:205], v179 offset:38912
	ds_read_b128 v[206:209], v180 offset:36864
	ds_read_b128 v[210:213], v180 offset:38912
	s_add_u32 s44, s44, s20
	s_addc_u32 s45, s45, s21
	s_mov_b32 m0, s59
	s_nop 0
	global_load_lds_dwordx4 v162, s[44:45]
	s_mov_b32 m0, s60
	s_nop 0
	global_load_lds_dwordx4 v166, s[44:45]
	ds_read_b128 v[214:217], v169 offset:49152
	ds_read_b128 v[218:221], v169 offset:51200
	ds_read_b128 v[222:225], v178 offset:49152
	ds_read_b128 v[226:229], v178 offset:51200
	s_waitcnt vmcnt(8)
	s_waitcnt lgkmcnt(0)
	s_barrier
	s_waitcnt lgkmcnt(0)
	s_setprio 1
	s_waitcnt lgkmcnt(7)
	v_mfma_f32_16x16x128_f8f6f4 v[18:21], v[146:149], v[182:185], v[18:21] cbsz:4 blgp:4
	s_waitcnt lgkmcnt(5)
	v_mfma_f32_16x16x128_f8f6f4 v[18:21], v[154:157], v[190:193], v[18:21] cbsz:4 blgp:4
	v_mfma_f32_16x16x128_f8f6f4 v[22:25], v[150:153], v[182:185], v[22:25] cbsz:4 blgp:4
	s_nop 0
	v_mfma_f32_16x16x128_f8f6f4 v[22:25], v[158:161], v[190:193], v[22:25] cbsz:4 blgp:4
	v_mfma_f32_16x16x128_f8f6f4 v[26:29], v[146:149], v[186:189], v[26:29] cbsz:4 blgp:4
	s_waitcnt lgkmcnt(4)
	v_mfma_f32_16x16x128_f8f6f4 v[26:29], v[154:157], v[194:197], v[26:29] cbsz:4 blgp:4
	v_mfma_f32_16x16x128_f8f6f4 v[30:33], v[150:153], v[186:189], v[30:33] cbsz:4 blgp:4
	s_nop 0
	v_mfma_f32_16x16x128_f8f6f4 v[30:33], v[158:161], v[194:197], v[30:33] cbsz:4 blgp:4
	s_waitcnt lgkmcnt(3)
	v_mfma_f32_16x16x128_f8f6f4 v[34:37], v[146:149], v[198:201], v[34:37] cbsz:4 blgp:4
	s_waitcnt lgkmcnt(1)
	v_mfma_f32_16x16x128_f8f6f4 v[34:37], v[154:157], v[206:209], v[34:37] cbsz:4 blgp:4
	v_mfma_f32_16x16x128_f8f6f4 v[38:41], v[150:153], v[198:201], v[38:41] cbsz:4 blgp:4
	s_nop 0
	v_mfma_f32_16x16x128_f8f6f4 v[38:41], v[158:161], v[206:209], v[38:41] cbsz:4 blgp:4
	v_mfma_f32_16x16x128_f8f6f4 v[42:45], v[146:149], v[202:205], v[42:45] cbsz:4 blgp:4
	s_waitcnt lgkmcnt(0)
	v_mfma_f32_16x16x128_f8f6f4 v[42:45], v[154:157], v[210:213], v[42:45] cbsz:4 blgp:4
	v_mfma_f32_16x16x128_f8f6f4 v[46:49], v[150:153], v[202:205], v[46:49] cbsz:4 blgp:4
	s_nop 0
	v_mfma_f32_16x16x128_f8f6f4 v[46:49], v[158:161], v[210:213], v[46:49] cbsz:4 blgp:4
	s_waitcnt lgkmcnt(3)
	v_mfma_f32_16x16x128_f8f6f4 v[50:53], v[214:217], v[182:185], v[50:53] cbsz:4 blgp:4
	s_waitcnt lgkmcnt(1)
	v_mfma_f32_16x16x128_f8f6f4 v[50:53], v[222:225], v[190:193], v[50:53] cbsz:4 blgp:4
	v_mfma_f32_16x16x128_f8f6f4 v[54:57], v[218:221], v[182:185], v[54:57] cbsz:4 blgp:4
	s_waitcnt lgkmcnt(0)
	v_mfma_f32_16x16x128_f8f6f4 v[54:57], v[226:229], v[190:193], v[54:57] cbsz:4 blgp:4
	v_mfma_f32_16x16x128_f8f6f4 v[58:61], v[214:217], v[186:189], v[58:61] cbsz:4 blgp:4
	s_nop 0
	v_mfma_f32_16x16x128_f8f6f4 v[58:61], v[222:225], v[194:197], v[58:61] cbsz:4 blgp:4
	v_mfma_f32_16x16x128_f8f6f4 v[62:65], v[218:221], v[186:189], v[62:65] cbsz:4 blgp:4
	s_nop 0
	v_mfma_f32_16x16x128_f8f6f4 v[62:65], v[226:229], v[194:197], v[62:65] cbsz:4 blgp:4
	v_mfma_f32_16x16x128_f8f6f4 v[66:69], v[214:217], v[198:201], v[66:69] cbsz:4 blgp:4
	s_nop 0
	v_mfma_f32_16x16x128_f8f6f4 v[66:69], v[222:225], v[206:209], v[66:69] cbsz:4 blgp:4
	v_mfma_f32_16x16x128_f8f6f4 v[70:73], v[218:221], v[198:201], v[70:73] cbsz:4 blgp:4
	s_nop 0
	v_mfma_f32_16x16x128_f8f6f4 v[70:73], v[226:229], v[206:209], v[70:73] cbsz:4 blgp:4
	v_mfma_f32_16x16x128_f8f6f4 v[74:77], v[214:217], v[202:205], v[74:77] cbsz:4 blgp:4
	s_nop 0
	v_mfma_f32_16x16x128_f8f6f4 v[74:77], v[222:225], v[210:213], v[74:77] cbsz:4 blgp:4
	v_mfma_f32_16x16x128_f8f6f4 v[78:81], v[218:221], v[202:205], v[78:81] cbsz:4 blgp:4
	s_nop 0
	v_mfma_f32_16x16x128_f8f6f4 v[78:81], v[226:229], v[210:213], v[78:81] cbsz:4 blgp:4
	s_setprio 0
	s_barrier
	s_mov_b32 m0, s62
	s_nop 0
	global_load_lds_dwordx4 v164, s[40:41]
	s_mov_b32 m0, s63
	s_nop 0
	global_load_lds_dwordx4 v168, s[40:41]
	ds_read_b128 v[182:185], v179 offset:49152
	ds_read_b128 v[186:189], v179 offset:51200
	ds_read_b128 v[190:193], v180 offset:49152
	ds_read_b128 v[194:197], v180 offset:51200
	ds_read_b128 v[198:201], v179 offset:53248
	ds_read_b128 v[202:205], v179 offset:55296
	ds_read_b128 v[206:209], v180 offset:53248
	ds_read_b128 v[210:213], v180 offset:55296
	s_mov_b32 m0, s64
	s_nop 0
	global_load_lds_dwordx4 v162, s[42:43]
	s_mov_b32 m0, s65
	s_nop 0
	global_load_lds_dwordx4 v166, s[42:43]
	s_add_u32 s40, s40, s22
	s_addc_u32 s41, s41, s23
	s_mov_b32 m0, s66
	s_nop 0
	global_load_lds_dwordx4 v164, s[40:41]
	s_mov_b32 m0, s67
	s_nop 0
	global_load_lds_dwordx4 v168, s[40:41]
	s_waitcnt vmcnt(8)
	s_waitcnt lgkmcnt(0)
	s_barrier
	s_setprio 1
	s_waitcnt lgkmcnt(7)
	v_mfma_f32_16x16x128_f8f6f4 v[86:89], v[146:149], v[182:185], v[86:89] cbsz:4 blgp:4
	s_waitcnt lgkmcnt(5)
	v_mfma_f32_16x16x128_f8f6f4 v[86:89], v[154:157], v[190:193], v[86:89] cbsz:4 blgp:4
	v_mfma_f32_16x16x128_f8f6f4 v[90:93], v[150:153], v[182:185], v[90:93] cbsz:4 blgp:4
	s_nop 0
	v_mfma_f32_16x16x128_f8f6f4 v[90:93], v[158:161], v[190:193], v[90:93] cbsz:4 blgp:4
	v_mfma_f32_16x16x128_f8f6f4 v[98:101], v[146:149], v[186:189], v[98:101] cbsz:4 blgp:4
	s_waitcnt lgkmcnt(4)
	v_mfma_f32_16x16x128_f8f6f4 v[98:101], v[154:157], v[194:197], v[98:101] cbsz:4 blgp:4
	v_mfma_f32_16x16x128_f8f6f4 v[106:109], v[150:153], v[186:189], v[106:109] cbsz:4 blgp:4
	s_nop 0
	v_mfma_f32_16x16x128_f8f6f4 v[106:109], v[158:161], v[194:197], v[106:109] cbsz:4 blgp:4
	s_waitcnt lgkmcnt(3)
	v_mfma_f32_16x16x128_f8f6f4 v[118:121], v[146:149], v[198:201], v[118:121] cbsz:4 blgp:4
	s_waitcnt lgkmcnt(1)
	v_mfma_f32_16x16x128_f8f6f4 v[118:121], v[154:157], v[206:209], v[118:121] cbsz:4 blgp:4
	v_mfma_f32_16x16x128_f8f6f4 v[126:129], v[150:153], v[198:201], v[126:129] cbsz:4 blgp:4
	s_nop 0
	v_mfma_f32_16x16x128_f8f6f4 v[126:129], v[158:161], v[206:209], v[126:129] cbsz:4 blgp:4
	v_mfma_f32_16x16x128_f8f6f4 v[138:141], v[146:149], v[202:205], v[138:141] cbsz:4 blgp:4
	s_waitcnt lgkmcnt(0)
	v_mfma_f32_16x16x128_f8f6f4 v[138:141], v[154:157], v[210:213], v[138:141] cbsz:4 blgp:4
	v_mfma_f32_16x16x128_f8f6f4 v[82:85], v[150:153], v[202:205], v[82:85] cbsz:4 blgp:4
	s_nop 0
	v_mfma_f32_16x16x128_f8f6f4 v[82:85], v[158:161], v[210:213], v[82:85] cbsz:4 blgp:4
	v_mfma_f32_16x16x128_f8f6f4 v[94:97], v[214:217], v[182:185], v[94:97] cbsz:4 blgp:4
	s_nop 0
	v_mfma_f32_16x16x128_f8f6f4 v[94:97], v[222:225], v[190:193], v[94:97] cbsz:4 blgp:4
	v_mfma_f32_16x16x128_f8f6f4 v[102:105], v[218:221], v[182:185], v[102:105] cbsz:4 blgp:4
	s_nop 0
	v_mfma_f32_16x16x128_f8f6f4 v[102:105], v[226:229], v[190:193], v[102:105] cbsz:4 blgp:4
	v_mfma_f32_16x16x128_f8f6f4 v[110:113], v[214:217], v[186:189], v[110:113] cbsz:4 blgp:4
	s_nop 0
	v_mfma_f32_16x16x128_f8f6f4 v[110:113], v[222:225], v[194:197], v[110:113] cbsz:4 blgp:4
	v_mfma_f32_16x16x128_f8f6f4 v[114:117], v[218:221], v[186:189], v[114:117] cbsz:4 blgp:4
	s_nop 0
	v_mfma_f32_16x16x128_f8f6f4 v[114:117], v[226:229], v[194:197], v[114:117] cbsz:4 blgp:4
	v_mfma_f32_16x16x128_f8f6f4 v[122:125], v[214:217], v[198:201], v[122:125] cbsz:4 blgp:4
	s_nop 0
	v_mfma_f32_16x16x128_f8f6f4 v[122:125], v[222:225], v[206:209], v[122:125] cbsz:4 blgp:4
	v_mfma_f32_16x16x128_f8f6f4 v[130:133], v[218:221], v[198:201], v[130:133] cbsz:4 blgp:4
	s_nop 0
	v_mfma_f32_16x16x128_f8f6f4 v[130:133], v[226:229], v[206:209], v[130:133] cbsz:4 blgp:4
	v_mfma_f32_16x16x128_f8f6f4 v[134:137], v[214:217], v[202:205], v[134:137] cbsz:4 blgp:4
	s_nop 0
	v_mfma_f32_16x16x128_f8f6f4 v[134:137], v[222:225], v[210:213], v[134:137] cbsz:4 blgp:4
	v_mfma_f32_16x16x128_f8f6f4 v[142:145], v[218:221], v[202:205], v[142:145] cbsz:4 blgp:4
	s_nop 0
	v_mfma_f32_16x16x128_f8f6f4 v[142:145], v[226:229], v[210:213], v[142:145] cbsz:4 blgp:4
	s_setprio 0
	s_andn2_b64 vcc, exec, s[28:29]
	s_barrier
	s_cbranch_vccnz .LBB6_20
	s_ashr_i32 s39, s38, 31
	s_lshl_b64 s[38:39], s[38:39], 10
	s_add_u32 s38, s14, s38
	s_addc_u32 s39, s15, s39
	s_add_u32 s31, s36, 0x200
	s_addc_u32 s46, s37, 0
	s_add_u32 s47, s34, 0x200
	s_addc_u32 s81, s35, 0
	s_add_u32 s34, s82, 0x180
	s_addc_u32 s35, s83, 0
	s_mov_b32 s82, 4
	s_cmp_eq_u32 s61, s82
	s_cselect_b64 s[36:37], -1, 0
	s_cmp_lg_u32 s61, s82
	s_cbranch_scc1 .LBB6_18

.LBB6_18:
	ds_read_b128 v[146:149], v169
	ds_read_b128 v[150:153], v169 offset:2048
	ds_read_b128 v[154:157], v178
	ds_read_b128 v[158:161], v178 offset:2048
	s_and_b64 s[36:37], s[36:37], exec
	s_cselect_b32 s42, s4, s31
	s_cselect_b32 s43, s5, s46
	s_cselect_b32 s45, s7, s81
	s_cselect_b32 s44, s6, s47
	s_add_u32 s40, s42, 0x80
	s_addc_u32 s41, s43, 0
	s_add_u32 s36, s44, 0x80
	s_addc_u32 s37, s45, 0
	ds_read_b128 v[182:185], v179
	ds_read_b128 v[186:189], v179 offset:2048
	ds_read_b128 v[190:193], v180
	ds_read_b128 v[194:197], v180 offset:2048
	ds_read_b128 v[198:201], v179 offset:4096
	ds_read_b128 v[202:205], v179 offset:6144
	ds_read_b128 v[206:209], v180 offset:4096
	ds_read_b128 v[210:213], v180 offset:6144
	s_mov_b32 m0, s68
	s_nop 0
	global_load_lds_dwordx4 v162, s[34:35]
	s_mov_b32 m0, s69
	s_nop 0
	global_load_lds_dwordx4 v166, s[34:35]
	ds_read_b128 v[214:217], v169 offset:16384
	ds_read_b128 v[218:221], v169 offset:18432
	ds_read_b128 v[222:225], v178 offset:16384
	ds_read_b128 v[226:229], v178 offset:18432
	s_waitcnt vmcnt(8)
	s_waitcnt lgkmcnt(0)
	s_barrier
	s_waitcnt lgkmcnt(0)
	s_setprio 1
	s_waitcnt lgkmcnt(7)
	v_mfma_f32_16x16x128_f8f6f4 v[18:21], v[146:149], v[182:185], v[18:21] cbsz:4 blgp:4
	s_waitcnt lgkmcnt(5)
	v_mfma_f32_16x16x128_f8f6f4 v[18:21], v[154:157], v[190:193], v[18:21] cbsz:4 blgp:4
	v_mfma_f32_16x16x128_f8f6f4 v[22:25], v[150:153], v[182:185], v[22:25] cbsz:4 blgp:4
	s_nop 0
	v_mfma_f32_16x16x128_f8f6f4 v[22:25], v[158:161], v[190:193], v[22:25] cbsz:4 blgp:4
	v_mfma_f32_16x16x128_f8f6f4 v[26:29], v[146:149], v[186:189], v[26:29] cbsz:4 blgp:4
	s_waitcnt lgkmcnt(4)
	v_mfma_f32_16x16x128_f8f6f4 v[26:29], v[154:157], v[194:197], v[26:29] cbsz:4 blgp:4
	v_mfma_f32_16x16x128_f8f6f4 v[30:33], v[150:153], v[186:189], v[30:33] cbsz:4 blgp:4
	s_nop 0
	v_mfma_f32_16x16x128_f8f6f4 v[30:33], v[158:161], v[194:197], v[30:33] cbsz:4 blgp:4
	s_waitcnt lgkmcnt(3)
	v_mfma_f32_16x16x128_f8f6f4 v[34:37], v[146:149], v[198:201], v[34:37] cbsz:4 blgp:4
	s_waitcnt lgkmcnt(1)
	v_mfma_f32_16x16x128_f8f6f4 v[34:37], v[154:157], v[206:209], v[34:37] cbsz:4 blgp:4
	v_mfma_f32_16x16x128_f8f6f4 v[38:41], v[150:153], v[198:201], v[38:41] cbsz:4 blgp:4
	s_nop 0
	v_mfma_f32_16x16x128_f8f6f4 v[38:41], v[158:161], v[206:209], v[38:41] cbsz:4 blgp:4
	v_mfma_f32_16x16x128_f8f6f4 v[42:45], v[146:149], v[202:205], v[42:45] cbsz:4 blgp:4
	s_waitcnt lgkmcnt(0)
	v_mfma_f32_16x16x128_f8f6f4 v[42:45], v[154:157], v[210:213], v[42:45] cbsz:4 blgp:4
	v_mfma_f32_16x16x128_f8f6f4 v[46:49], v[150:153], v[202:205], v[46:49] cbsz:4 blgp:4
	s_nop 0
	v_mfma_f32_16x16x128_f8f6f4 v[46:49], v[158:161], v[210:213], v[46:49] cbsz:4 blgp:4
	s_waitcnt lgkmcnt(3)
	v_mfma_f32_16x16x128_f8f6f4 v[50:53], v[214:217], v[182:185], v[50:53] cbsz:4 blgp:4
	s_waitcnt lgkmcnt(1)
	v_mfma_f32_16x16x128_f8f6f4 v[50:53], v[222:225], v[190:193], v[50:53] cbsz:4 blgp:4
	v_mfma_f32_16x16x128_f8f6f4 v[54:57], v[218:221], v[182:185], v[54:57] cbsz:4 blgp:4
	s_waitcnt lgkmcnt(0)
	v_mfma_f32_16x16x128_f8f6f4 v[54:57], v[226:229], v[190:193], v[54:57] cbsz:4 blgp:4
	v_mfma_f32_16x16x128_f8f6f4 v[58:61], v[214:217], v[186:189], v[58:61] cbsz:4 blgp:4
	s_nop 0
	v_mfma_f32_16x16x128_f8f6f4 v[58:61], v[222:225], v[194:197], v[58:61] cbsz:4 blgp:4
	v_mfma_f32_16x16x128_f8f6f4 v[62:65], v[218:221], v[186:189], v[62:65] cbsz:4 blgp:4
	s_nop 0
	v_mfma_f32_16x16x128_f8f6f4 v[62:65], v[226:229], v[194:197], v[62:65] cbsz:4 blgp:4
	v_mfma_f32_16x16x128_f8f6f4 v[66:69], v[214:217], v[198:201], v[66:69] cbsz:4 blgp:4
	s_nop 0
	v_mfma_f32_16x16x128_f8f6f4 v[66:69], v[222:225], v[206:209], v[66:69] cbsz:4 blgp:4
	v_mfma_f32_16x16x128_f8f6f4 v[70:73], v[218:221], v[198:201], v[70:73] cbsz:4 blgp:4
	s_nop 0
	v_mfma_f32_16x16x128_f8f6f4 v[70:73], v[226:229], v[206:209], v[70:73] cbsz:4 blgp:4
	v_mfma_f32_16x16x128_f8f6f4 v[74:77], v[214:217], v[202:205], v[74:77] cbsz:4 blgp:4
	s_nop 0
	v_mfma_f32_16x16x128_f8f6f4 v[74:77], v[222:225], v[210:213], v[74:77] cbsz:4 blgp:4
	v_mfma_f32_16x16x128_f8f6f4 v[78:81], v[218:221], v[202:205], v[78:81] cbsz:4 blgp:4
	s_nop 0
	v_mfma_f32_16x16x128_f8f6f4 v[78:81], v[226:229], v[210:213], v[78:81] cbsz:4 blgp:4
	s_setprio 0
	s_barrier
	s_mov_b32 m0, s54
	s_nop 0
	global_load_lds_dwordx4 v164, s[44:45]
	s_mov_b32 m0, s55
	s_nop 0
	global_load_lds_dwordx4 v168, s[44:45]
	ds_read_b128 v[182:185], v179 offset:16384
	ds_read_b128 v[186:189], v179 offset:18432
	ds_read_b128 v[190:193], v180 offset:16384
	ds_read_b128 v[194:197], v180 offset:18432
	ds_read_b128 v[198:201], v179 offset:20480
	ds_read_b128 v[202:205], v179 offset:22528
	ds_read_b128 v[206:209], v180 offset:20480
	ds_read_b128 v[210:213], v180 offset:22528
	s_mov_b32 m0, s53
	s_nop 0
	global_load_lds_dwordx4 v162, s[42:43]
	s_mov_b32 m0, s56
	s_nop 0
	global_load_lds_dwordx4 v166, s[42:43]
	s_add_u32 s44, s44, s22
	s_addc_u32 s45, s45, s23
	s_mov_b32 m0, s57
	s_nop 0
	global_load_lds_dwordx4 v164, s[44:45]
	s_mov_b32 m0, s58
	s_nop 0
	global_load_lds_dwordx4 v168, s[44:45]
	s_waitcnt vmcnt(8)
	s_waitcnt lgkmcnt(0)
	s_barrier
	s_setprio 1
	s_waitcnt lgkmcnt(7)
	v_mfma_f32_16x16x128_f8f6f4 v[86:89], v[146:149], v[182:185], v[86:89] cbsz:4 blgp:4
	s_waitcnt lgkmcnt(5)
	v_mfma_f32_16x16x128_f8f6f4 v[86:89], v[154:157], v[190:193], v[86:89] cbsz:4 blgp:4
	v_mfma_f32_16x16x128_f8f6f4 v[90:93], v[150:153], v[182:185], v[90:93] cbsz:4 blgp:4
	s_nop 0
	v_mfma_f32_16x16x128_f8f6f4 v[90:93], v[158:161], v[190:193], v[90:93] cbsz:4 blgp:4
	v_mfma_f32_16x16x128_f8f6f4 v[98:101], v[146:149], v[186:189], v[98:101] cbsz:4 blgp:4
	s_waitcnt lgkmcnt(4)
	v_mfma_f32_16x16x128_f8f6f4 v[98:101], v[154:157], v[194:197], v[98:101] cbsz:4 blgp:4
	v_mfma_f32_16x16x128_f8f6f4 v[106:109], v[150:153], v[186:189], v[106:109] cbsz:4 blgp:4
	s_nop 0
	v_mfma_f32_16x16x128_f8f6f4 v[106:109], v[158:161], v[194:197], v[106:109] cbsz:4 blgp:4
	s_waitcnt lgkmcnt(3)
	v_mfma_f32_16x16x128_f8f6f4 v[118:121], v[146:149], v[198:201], v[118:121] cbsz:4 blgp:4
	s_waitcnt lgkmcnt(1)
	v_mfma_f32_16x16x128_f8f6f4 v[118:121], v[154:157], v[206:209], v[118:121] cbsz:4 blgp:4
	v_mfma_f32_16x16x128_f8f6f4 v[126:129], v[150:153], v[198:201], v[126:129] cbsz:4 blgp:4
	s_nop 0
	v_mfma_f32_16x16x128_f8f6f4 v[126:129], v[158:161], v[206:209], v[126:129] cbsz:4 blgp:4
	v_mfma_f32_16x16x128_f8f6f4 v[138:141], v[146:149], v[202:205], v[138:141] cbsz:4 blgp:4
	s_waitcnt lgkmcnt(0)
	v_mfma_f32_16x16x128_f8f6f4 v[138:141], v[154:157], v[210:213], v[138:141] cbsz:4 blgp:4
	v_mfma_f32_16x16x128_f8f6f4 v[82:85], v[150:153], v[202:205], v[82:85] cbsz:4 blgp:4
	s_nop 0
	v_mfma_f32_16x16x128_f8f6f4 v[82:85], v[158:161], v[210:213], v[82:85] cbsz:4 blgp:4
	v_mfma_f32_16x16x128_f8f6f4 v[94:97], v[214:217], v[182:185], v[94:97] cbsz:4 blgp:4
	s_nop 0
	v_mfma_f32_16x16x128_f8f6f4 v[94:97], v[222:225], v[190:193], v[94:97] cbsz:4 blgp:4
	v_mfma_f32_16x16x128_f8f6f4 v[102:105], v[218:221], v[182:185], v[102:105] cbsz:4 blgp:4
	s_nop 0
	v_mfma_f32_16x16x128_f8f6f4 v[102:105], v[226:229], v[190:193], v[102:105] cbsz:4 blgp:4
	v_mfma_f32_16x16x128_f8f6f4 v[110:113], v[214:217], v[186:189], v[110:113] cbsz:4 blgp:4
	s_nop 0
	v_mfma_f32_16x16x128_f8f6f4 v[110:113], v[222:225], v[194:197], v[110:113] cbsz:4 blgp:4
	v_mfma_f32_16x16x128_f8f6f4 v[114:117], v[218:221], v[186:189], v[114:117] cbsz:4 blgp:4
	s_nop 0
	v_mfma_f32_16x16x128_f8f6f4 v[114:117], v[226:229], v[194:197], v[114:117] cbsz:4 blgp:4
	v_mfma_f32_16x16x128_f8f6f4 v[122:125], v[214:217], v[198:201], v[122:125] cbsz:4 blgp:4
	s_nop 0
	v_mfma_f32_16x16x128_f8f6f4 v[122:125], v[222:225], v[206:209], v[122:125] cbsz:4 blgp:4
	v_mfma_f32_16x16x128_f8f6f4 v[130:133], v[218:221], v[198:201], v[130:133] cbsz:4 blgp:4
	s_nop 0
	v_mfma_f32_16x16x128_f8f6f4 v[130:133], v[226:229], v[206:209], v[130:133] cbsz:4 blgp:4
	v_mfma_f32_16x16x128_f8f6f4 v[134:137], v[214:217], v[202:205], v[134:137] cbsz:4 blgp:4
	s_nop 0
	v_mfma_f32_16x16x128_f8f6f4 v[134:137], v[222:225], v[210:213], v[134:137] cbsz:4 blgp:4
	v_mfma_f32_16x16x128_f8f6f4 v[142:145], v[218:221], v[202:205], v[142:145] cbsz:4 blgp:4
	s_nop 0
	v_mfma_f32_16x16x128_f8f6f4 v[142:145], v[226:229], v[210:213], v[142:145] cbsz:4 blgp:4
	s_setprio 0
	s_barrier
	ds_read_b128 v[146:149], v169 offset:32768
	ds_read_b128 v[150:153], v169 offset:34816
	ds_read_b128 v[154:157], v178 offset:32768
	ds_read_b128 v[158:161], v178 offset:34816
	ds_read_b128 v[182:185], v179 offset:32768
	ds_read_b128 v[186:189], v179 offset:34816
	ds_read_b128 v[190:193], v180 offset:32768
	ds_read_b128 v[194:197], v180 offset:34816
	ds_read_b128 v[198:201], v179 offset:36864
	ds_read_b128 v[202:205], v179 offset:38912
	ds_read_b128 v[206:209], v180 offset:36864
	ds_read_b128 v[210:213], v180 offset:38912
	s_add_u32 s42, s42, s20
	s_addc_u32 s43, s43, s21
	s_mov_b32 m0, s59
	s_nop 0
	global_load_lds_dwordx4 v162, s[42:43]
	s_mov_b32 m0, s60
	s_nop 0
	global_load_lds_dwordx4 v166, s[42:43]
	ds_read_b128 v[214:217], v169 offset:49152
	ds_read_b128 v[218:221], v169 offset:51200
	ds_read_b128 v[222:225], v178 offset:49152
	ds_read_b128 v[226:229], v178 offset:51200
	s_waitcnt vmcnt(8)
	s_waitcnt lgkmcnt(0)
	s_barrier
	s_waitcnt lgkmcnt(0)
	s_setprio 1
	s_waitcnt lgkmcnt(7)
	v_mfma_f32_16x16x128_f8f6f4 v[18:21], v[146:149], v[182:185], v[18:21] cbsz:4 blgp:4
	s_waitcnt lgkmcnt(5)
	v_mfma_f32_16x16x128_f8f6f4 v[18:21], v[154:157], v[190:193], v[18:21] cbsz:4 blgp:4
	v_mfma_f32_16x16x128_f8f6f4 v[22:25], v[150:153], v[182:185], v[22:25] cbsz:4 blgp:4
	s_nop 0
	v_mfma_f32_16x16x128_f8f6f4 v[22:25], v[158:161], v[190:193], v[22:25] cbsz:4 blgp:4
	v_mfma_f32_16x16x128_f8f6f4 v[26:29], v[146:149], v[186:189], v[26:29] cbsz:4 blgp:4
	s_waitcnt lgkmcnt(4)
	v_mfma_f32_16x16x128_f8f6f4 v[26:29], v[154:157], v[194:197], v[26:29] cbsz:4 blgp:4
	v_mfma_f32_16x16x128_f8f6f4 v[30:33], v[150:153], v[186:189], v[30:33] cbsz:4 blgp:4
	s_nop 0
	v_mfma_f32_16x16x128_f8f6f4 v[30:33], v[158:161], v[194:197], v[30:33] cbsz:4 blgp:4
	s_waitcnt lgkmcnt(3)
	v_mfma_f32_16x16x128_f8f6f4 v[34:37], v[146:149], v[198:201], v[34:37] cbsz:4 blgp:4
	s_waitcnt lgkmcnt(1)
	v_mfma_f32_16x16x128_f8f6f4 v[34:37], v[154:157], v[206:209], v[34:37] cbsz:4 blgp:4
	v_mfma_f32_16x16x128_f8f6f4 v[38:41], v[150:153], v[198:201], v[38:41] cbsz:4 blgp:4
	s_nop 0
	v_mfma_f32_16x16x128_f8f6f4 v[38:41], v[158:161], v[206:209], v[38:41] cbsz:4 blgp:4
	v_mfma_f32_16x16x128_f8f6f4 v[42:45], v[146:149], v[202:205], v[42:45] cbsz:4 blgp:4
	s_waitcnt lgkmcnt(0)
	v_mfma_f32_16x16x128_f8f6f4 v[42:45], v[154:157], v[210:213], v[42:45] cbsz:4 blgp:4
	v_mfma_f32_16x16x128_f8f6f4 v[46:49], v[150:153], v[202:205], v[46:49] cbsz:4 blgp:4
	s_nop 0
	v_mfma_f32_16x16x128_f8f6f4 v[46:49], v[158:161], v[210:213], v[46:49] cbsz:4 blgp:4
	s_waitcnt lgkmcnt(3)
	v_mfma_f32_16x16x128_f8f6f4 v[50:53], v[214:217], v[182:185], v[50:53] cbsz:4 blgp:4
	s_waitcnt lgkmcnt(1)
	v_mfma_f32_16x16x128_f8f6f4 v[50:53], v[222:225], v[190:193], v[50:53] cbsz:4 blgp:4
	v_mfma_f32_16x16x128_f8f6f4 v[54:57], v[218:221], v[182:185], v[54:57] cbsz:4 blgp:4
	s_waitcnt lgkmcnt(0)
	v_mfma_f32_16x16x128_f8f6f4 v[54:57], v[226:229], v[190:193], v[54:57] cbsz:4 blgp:4
	v_mfma_f32_16x16x128_f8f6f4 v[58:61], v[214:217], v[186:189], v[58:61] cbsz:4 blgp:4
	s_nop 0
	v_mfma_f32_16x16x128_f8f6f4 v[58:61], v[222:225], v[194:197], v[58:61] cbsz:4 blgp:4
	v_mfma_f32_16x16x128_f8f6f4 v[62:65], v[218:221], v[186:189], v[62:65] cbsz:4 blgp:4
	s_nop 0
	v_mfma_f32_16x16x128_f8f6f4 v[62:65], v[226:229], v[194:197], v[62:65] cbsz:4 blgp:4
	v_mfma_f32_16x16x128_f8f6f4 v[66:69], v[214:217], v[198:201], v[66:69] cbsz:4 blgp:4
	s_nop 0
	v_mfma_f32_16x16x128_f8f6f4 v[66:69], v[222:225], v[206:209], v[66:69] cbsz:4 blgp:4
	v_mfma_f32_16x16x128_f8f6f4 v[70:73], v[218:221], v[198:201], v[70:73] cbsz:4 blgp:4
	s_nop 0
	v_mfma_f32_16x16x128_f8f6f4 v[70:73], v[226:229], v[206:209], v[70:73] cbsz:4 blgp:4
	v_mfma_f32_16x16x128_f8f6f4 v[74:77], v[214:217], v[202:205], v[74:77] cbsz:4 blgp:4
	s_nop 0
	v_mfma_f32_16x16x128_f8f6f4 v[74:77], v[222:225], v[210:213], v[74:77] cbsz:4 blgp:4
	v_mfma_f32_16x16x128_f8f6f4 v[78:81], v[218:221], v[202:205], v[78:81] cbsz:4 blgp:4
	s_nop 0
	v_mfma_f32_16x16x128_f8f6f4 v[78:81], v[226:229], v[210:213], v[78:81] cbsz:4 blgp:4
	s_setprio 0
	s_barrier
	s_mov_b32 m0, s62
	s_nop 0
	global_load_lds_dwordx4 v164, s[36:37]
	s_mov_b32 m0, s63
	s_nop 0
	global_load_lds_dwordx4 v168, s[36:37]
	ds_read_b128 v[182:185], v179 offset:49152
	ds_read_b128 v[186:189], v179 offset:51200
	ds_read_b128 v[190:193], v180 offset:49152
	ds_read_b128 v[194:197], v180 offset:51200
	ds_read_b128 v[198:201], v179 offset:53248
	ds_read_b128 v[202:205], v179 offset:55296
	ds_read_b128 v[206:209], v180 offset:53248
	ds_read_b128 v[210:213], v180 offset:55296
	s_mov_b32 m0, s64
	s_nop 0
	global_load_lds_dwordx4 v162, s[40:41]
	s_mov_b32 m0, s65
	s_nop 0
	global_load_lds_dwordx4 v166, s[40:41]
	s_add_u32 s36, s36, s22
	s_addc_u32 s37, s37, s23
	s_mov_b32 m0, s66
	s_nop 0
	global_load_lds_dwordx4 v164, s[36:37]
	s_mov_b32 m0, s67
	s_nop 0
	global_load_lds_dwordx4 v168, s[36:37]
	s_waitcnt vmcnt(8)
	s_waitcnt lgkmcnt(0)
	s_barrier
	s_setprio 1
	s_waitcnt lgkmcnt(7)
	v_mfma_f32_16x16x128_f8f6f4 v[86:89], v[146:149], v[182:185], v[86:89] cbsz:4 blgp:4
	s_waitcnt lgkmcnt(5)
	v_mfma_f32_16x16x128_f8f6f4 v[86:89], v[154:157], v[190:193], v[86:89] cbsz:4 blgp:4
	v_mfma_f32_16x16x128_f8f6f4 v[90:93], v[150:153], v[182:185], v[90:93] cbsz:4 blgp:4
	s_nop 0
	v_mfma_f32_16x16x128_f8f6f4 v[90:93], v[158:161], v[190:193], v[90:93] cbsz:4 blgp:4
	v_mfma_f32_16x16x128_f8f6f4 v[98:101], v[146:149], v[186:189], v[98:101] cbsz:4 blgp:4
	s_waitcnt lgkmcnt(4)
	v_mfma_f32_16x16x128_f8f6f4 v[98:101], v[154:157], v[194:197], v[98:101] cbsz:4 blgp:4
	v_mfma_f32_16x16x128_f8f6f4 v[106:109], v[150:153], v[186:189], v[106:109] cbsz:4 blgp:4
	s_nop 0
	v_mfma_f32_16x16x128_f8f6f4 v[106:109], v[158:161], v[194:197], v[106:109] cbsz:4 blgp:4
	s_waitcnt lgkmcnt(3)
	v_mfma_f32_16x16x128_f8f6f4 v[118:121], v[146:149], v[198:201], v[118:121] cbsz:4 blgp:4
	s_waitcnt lgkmcnt(1)
	v_mfma_f32_16x16x128_f8f6f4 v[118:121], v[154:157], v[206:209], v[118:121] cbsz:4 blgp:4
	v_mfma_f32_16x16x128_f8f6f4 v[126:129], v[150:153], v[198:201], v[126:129] cbsz:4 blgp:4
	s_nop 0
	v_mfma_f32_16x16x128_f8f6f4 v[126:129], v[158:161], v[206:209], v[126:129] cbsz:4 blgp:4
	v_mfma_f32_16x16x128_f8f6f4 v[138:141], v[146:149], v[202:205], v[138:141] cbsz:4 blgp:4
	s_waitcnt lgkmcnt(0)
	v_mfma_f32_16x16x128_f8f6f4 v[138:141], v[154:157], v[210:213], v[138:141] cbsz:4 blgp:4
	v_mfma_f32_16x16x128_f8f6f4 v[82:85], v[150:153], v[202:205], v[82:85] cbsz:4 blgp:4
	s_nop 0
	v_mfma_f32_16x16x128_f8f6f4 v[82:85], v[158:161], v[210:213], v[82:85] cbsz:4 blgp:4
	v_mfma_f32_16x16x128_f8f6f4 v[94:97], v[214:217], v[182:185], v[94:97] cbsz:4 blgp:4
	s_nop 0
	v_mfma_f32_16x16x128_f8f6f4 v[94:97], v[222:225], v[190:193], v[94:97] cbsz:4 blgp:4
	v_mfma_f32_16x16x128_f8f6f4 v[102:105], v[218:221], v[182:185], v[102:105] cbsz:4 blgp:4
	s_nop 0
	v_mfma_f32_16x16x128_f8f6f4 v[102:105], v[226:229], v[190:193], v[102:105] cbsz:4 blgp:4
	v_mfma_f32_16x16x128_f8f6f4 v[110:113], v[214:217], v[186:189], v[110:113] cbsz:4 blgp:4
	s_nop 0
	v_mfma_f32_16x16x128_f8f6f4 v[110:113], v[222:225], v[194:197], v[110:113] cbsz:4 blgp:4
	v_mfma_f32_16x16x128_f8f6f4 v[114:117], v[218:221], v[186:189], v[114:117] cbsz:4 blgp:4
	s_nop 0
	v_mfma_f32_16x16x128_f8f6f4 v[114:117], v[226:229], v[194:197], v[114:117] cbsz:4 blgp:4
	v_mfma_f32_16x16x128_f8f6f4 v[122:125], v[214:217], v[198:201], v[122:125] cbsz:4 blgp:4
	s_nop 0
	v_mfma_f32_16x16x128_f8f6f4 v[122:125], v[222:225], v[206:209], v[122:125] cbsz:4 blgp:4
	v_mfma_f32_16x16x128_f8f6f4 v[130:133], v[218:221], v[198:201], v[130:133] cbsz:4 blgp:4
	s_nop 0
	v_mfma_f32_16x16x128_f8f6f4 v[130:133], v[226:229], v[206:209], v[130:133] cbsz:4 blgp:4
	v_mfma_f32_16x16x128_f8f6f4 v[134:137], v[214:217], v[202:205], v[134:137] cbsz:4 blgp:4
	s_nop 0
	v_mfma_f32_16x16x128_f8f6f4 v[134:137], v[222:225], v[210:213], v[134:137] cbsz:4 blgp:4
	v_mfma_f32_16x16x128_f8f6f4 v[142:145], v[218:221], v[202:205], v[142:145] cbsz:4 blgp:4
	s_nop 0
	v_mfma_f32_16x16x128_f8f6f4 v[142:145], v[226:229], v[210:213], v[142:145] cbsz:4 blgp:4
	s_setprio 0
	s_add_i32 s36, s82, 2
	s_add_u32 s31, s31, 0x100
	s_addc_u32 s46, s46, 0
	s_add_u32 s47, s47, 0x100
	s_addc_u32 s81, s81, 0
	s_add_u32 s34, s34, 0x100
	s_addc_u32 s35, s35, 0
	s_cmp_ge_i32 s82, s61
	s_barrier
	s_cbranch_scc1 .LBB6_20
	s_mov_b32 s82, s36
	s_cmp_eq_u32 s61, s82
	s_cselect_b64 s[36:37], -1, 0
	s_cmp_lg_u32 s61, s82
	s_cbranch_scc0 .LBB6_17
	s_branch .LBB6_18
